# speedup vs baseline: 1.0029x; 1.0029x over previous
.Lk4_st1_6:
	s_add_u32 s52, s10, 0x800000
	s_addc_u32 s53, s11, 0
	v_lshlrev_b32_e32 v169, 2, v98
	v_lshlrev_b32_e32 v170, 2, v100
	global_load_dwordx4 v[128:131], v169, s[52:53] nt
	global_load_dwordx4 v[132:135], v170, s[52:53] nt
	s_add_u32 s52, s10, 0xc00000
	s_addc_u32 s53, s11, 0
	v_lshlrev_b32_e32 v169, 2, v94
	v_lshlrev_b32_e32 v170, 2, v96
	global_load_dwordx4 v[172:175], v169, s[52:53] nt
	global_load_dwordx4 v[176:179], v170, s[52:53] nt
	s_add_u32 s52, s10, 0x1000000
	s_addc_u32 s53, s11, 0
	v_lshlrev_b32_e32 v169, 2, v94
	global_load_dwordx4 v[124:127], v169, s[52:53] nt
	v_mfma_f32_16x16x32_f16 a[0:3], v[70:73], v[82:85], a[0:3]
	ds_read_b128 v[14:17], v144
	v_mfma_f32_16x16x32_f16 a[4:7], v[70:73], v[86:89], a[4:7]
	ds_read_b128 v[18:21], v146
	v_mfma_f32_16x16x32_f16 a[12:15], v[66:69], v[82:85], a[12:15]
	ds_read_b128 v[42:45], v166
	v_mfma_f32_16x16x32_f16 a[16:19], v[66:69], v[86:89], a[16:19]
	ds_read_b128 v[38:41], v166 offset:1024
	v_mfma_f32_16x16x32_f16 a[28:31], v[58:61], v[82:85], a[28:31]
	ds_read_b128 v[34:37], v166 offset:2048
	v_mfma_f32_16x16x32_f16 a[60:63], v[58:61], v[86:89], a[60:63]
	ds_read_b128 v[30:33], v166 offset:3072
	v_mfma_f32_16x16x32_f16 a[8:11], v[54:57], v[82:85], a[8:11]
	ds_read_b128 v[26:29], v166 offset:4096
	v_mfma_f32_16x16x32_f16 a[20:23], v[54:57], v[86:89], a[20:23]
	ds_read_b128 v[22:25], v166 offset:5120
	v_mfma_f32_16x16x32_f16 a[24:27], v[46:49], v[82:85], a[24:27]
	ds_read_b128 v[10:13], v166 offset:6144
	v_mfma_f32_16x16x32_f16 a[36:39], v[46:49], v[86:89], a[36:39]
	ds_read_b128 v[6:9], v166 offset:7168
	v_mfma_f32_16x16x32_f16 a[44:47], v[50:53], v[82:85], a[44:47]
	ds_read_b128 v[2:5], v166 offset:8192
	v_mfma_f32_16x16x32_f16 a[64:67], v[50:53], v[86:89], a[64:67]
	v_mfma_f32_16x16x32_f16 a[32:35], v[62:65], v[82:85], a[32:35]
	v_mfma_f32_16x16x32_f16 a[40:43], v[62:65], v[86:89], a[40:43]
	v_mfma_f32_16x16x32_f16 a[48:51], v[74:77], v[82:85], a[48:51]
	v_mfma_f32_16x16x32_f16 a[52:55], v[74:77], v[86:89], a[52:55]
	v_mfma_f32_16x16x32_f16 a[56:59], v[78:81], v[82:85], a[56:59]
	v_mfma_f32_16x16x32_f16 a[68:71], v[78:81], v[86:89], a[68:71]
	s_waitcnt lgkmcnt(8)
	v_mfma_f32_16x16x32_f16 a[0:3], v[42:45], v[14:17], a[0:3]
	ds_read_b128 v[82:85], v145
	v_mfma_f32_16x16x32_f16 a[4:7], v[42:45], v[18:21], a[4:7]
	ds_read_b128 v[86:89], v147
	s_waitcnt lgkmcnt(9)
	v_mfma_f32_16x16x32_f16 a[12:15], v[38:41], v[14:17], a[12:15]
	ds_read_b128 v[70:73], v166 offset:9216
	v_mfma_f32_16x16x32_f16 a[16:19], v[38:41], v[18:21], a[16:19]
	ds_read_b128 v[66:69], v166 offset:10240
	s_waitcnt lgkmcnt(10)
	v_mfma_f32_16x16x32_f16 a[28:31], v[34:37], v[14:17], a[28:31]
	ds_read_b128 v[58:61], v166 offset:11264
	v_mfma_f32_16x16x32_f16 a[60:63], v[34:37], v[18:21], a[60:63]
	ds_read_b128 v[54:57], v166 offset:12288
	s_waitcnt lgkmcnt(11)
	v_mfma_f32_16x16x32_f16 a[8:11], v[30:33], v[14:17], a[8:11]
	ds_read_b128 v[46:49], v166 offset:13312
	v_mfma_f32_16x16x32_f16 a[20:23], v[30:33], v[18:21], a[20:23]
	ds_read_b128 v[50:53], v166 offset:14336
	s_waitcnt lgkmcnt(12)
	v_mfma_f32_16x16x32_f16 a[24:27], v[26:29], v[14:17], a[24:27]
	ds_read_b128 v[62:65], v166 offset:15360
	v_mfma_f32_16x16x32_f16 a[36:39], v[26:29], v[18:21], a[36:39]
	ds_read_b128 v[74:77], v166 offset:16384
	s_waitcnt lgkmcnt(13)
	v_mfma_f32_16x16x32_f16 a[44:47], v[22:25], v[14:17], a[44:47]
	ds_read_b128 v[78:81], v166 offset:17408
	v_mfma_f32_16x16x32_f16 a[64:67], v[22:25], v[18:21], a[64:67]
	s_waitcnt lgkmcnt(13)
	v_mfma_f32_16x16x32_f16 a[32:35], v[10:13], v[14:17], a[32:35]
	v_mfma_f32_16x16x32_f16 a[40:43], v[10:13], v[18:21], a[40:43]
	s_waitcnt lgkmcnt(12)
	v_mfma_f32_16x16x32_f16 a[48:51], v[6:9], v[14:17], a[48:51]
	v_mfma_f32_16x16x32_f16 a[52:55], v[6:9], v[18:21], a[52:55]
	s_waitcnt lgkmcnt(11)
	v_mfma_f32_16x16x32_f16 a[56:59], v[2:5], v[14:17], a[56:59]
	v_mfma_f32_16x16x32_f16 a[68:71], v[2:5], v[18:21], a[68:71]
	s_waitcnt lgkmcnt(8)
	v_mfma_f32_16x16x32_f16 a[0:3], v[70:73], v[82:85], a[0:3]
	ds_read_b128 v[14:17], v148
	v_mfma_f32_16x16x32_f16 a[4:7], v[70:73], v[86:89], a[4:7]
	ds_read_b128 v[18:21], v150
	s_waitcnt lgkmcnt(9)
	v_mfma_f32_16x16x32_f16 a[12:15], v[66:69], v[82:85], a[12:15]
	ds_read_b128 v[42:45], v167
	v_mfma_f32_16x16x32_f16 a[16:19], v[66:69], v[86:89], a[16:19]
	ds_read_b128 v[38:41], v167 offset:1024
	s_waitcnt lgkmcnt(10)
	v_mfma_f32_16x16x32_f16 a[28:31], v[58:61], v[82:85], a[28:31]
	ds_read_b128 v[34:37], v167 offset:2048
	v_mfma_f32_16x16x32_f16 a[60:63], v[58:61], v[86:89], a[60:63]
	ds_read_b128 v[30:33], v167 offset:3072
	s_waitcnt lgkmcnt(11)
	v_mfma_f32_16x16x32_f16 a[8:11], v[54:57], v[82:85], a[8:11]
	ds_read_b128 v[26:29], v167 offset:4096
	v_mfma_f32_16x16x32_f16 a[20:23], v[54:57], v[86:89], a[20:23]
	ds_read_b128 v[22:25], v167 offset:5120
	s_waitcnt lgkmcnt(12)
	v_mfma_f32_16x16x32_f16 a[24:27], v[46:49], v[82:85], a[24:27]
	ds_read_b128 v[10:13], v167 offset:6144
	v_mfma_f32_16x16x32_f16 a[36:39], v[46:49], v[86:89], a[36:39]
	ds_read_b128 v[6:9], v167 offset:7168
	s_waitcnt lgkmcnt(13)
	v_mfma_f32_16x16x32_f16 a[44:47], v[50:53], v[82:85], a[44:47]
	ds_read_b128 v[2:5], v167 offset:8192
	v_mfma_f32_16x16x32_f16 a[64:67], v[50:53], v[86:89], a[64:67]
	s_waitcnt lgkmcnt(13)
	v_mfma_f32_16x16x32_f16 a[32:35], v[62:65], v[82:85], a[32:35]
	v_mfma_f32_16x16x32_f16 a[40:43], v[62:65], v[86:89], a[40:43]
	s_waitcnt lgkmcnt(12)
	v_mfma_f32_16x16x32_f16 a[48:51], v[74:77], v[82:85], a[48:51]
	v_mfma_f32_16x16x32_f16 a[52:55], v[74:77], v[86:89], a[52:55]
	s_waitcnt lgkmcnt(11)
	v_mfma_f32_16x16x32_f16 a[56:59], v[78:81], v[82:85], a[56:59]
	v_mfma_f32_16x16x32_f16 a[68:71], v[78:81], v[86:89], a[68:71]
	s_waitcnt lgkmcnt(8)
	v_mfma_f32_16x16x32_f16 a[0:3], v[42:45], v[14:17], a[0:3]
	ds_read_b128 v[82:85], v149
	v_mfma_f32_16x16x32_f16 a[4:7], v[42:45], v[18:21], a[4:7]
	ds_read_b128 v[86:89], v151
	s_waitcnt lgkmcnt(9)
	v_mfma_f32_16x16x32_f16 a[12:15], v[38:41], v[14:17], a[12:15]
	ds_read_b128 v[70:73], v167 offset:9216
	v_mfma_f32_16x16x32_f16 a[16:19], v[38:41], v[18:21], a[16:19]
	ds_read_b128 v[66:69], v167 offset:10240
	s_waitcnt lgkmcnt(10)
	v_mfma_f32_16x16x32_f16 a[28:31], v[34:37], v[14:17], a[28:31]
	ds_read_b128 v[58:61], v167 offset:11264
	v_mfma_f32_16x16x32_f16 a[60:63], v[34:37], v[18:21], a[60:63]
	ds_read_b128 v[54:57], v167 offset:12288
	s_waitcnt lgkmcnt(11)
	v_mfma_f32_16x16x32_f16 a[8:11], v[30:33], v[14:17], a[8:11]
	ds_read_b128 v[46:49], v167 offset:13312
	v_mfma_f32_16x16x32_f16 a[20:23], v[30:33], v[18:21], a[20:23]
	ds_read_b128 v[50:53], v167 offset:14336
	s_waitcnt lgkmcnt(12)
	v_mfma_f32_16x16x32_f16 a[24:27], v[26:29], v[14:17], a[24:27]
	ds_read_b128 v[62:65], v167 offset:15360
	v_mfma_f32_16x16x32_f16 a[36:39], v[26:29], v[18:21], a[36:39]
	ds_read_b128 v[74:77], v167 offset:16384
	s_waitcnt lgkmcnt(13)
	v_mfma_f32_16x16x32_f16 a[44:47], v[22:25], v[14:17], a[44:47]
	ds_read_b128 v[78:81], v167 offset:17408
	v_mfma_f32_16x16x32_f16 a[64:67], v[22:25], v[18:21], a[64:67]
	s_waitcnt lgkmcnt(13)
	v_mfma_f32_16x16x32_f16 a[32:35], v[10:13], v[14:17], a[32:35]
	v_mfma_f32_16x16x32_f16 a[40:43], v[10:13], v[18:21], a[40:43]
	s_waitcnt lgkmcnt(12)
	v_mfma_f32_16x16x32_f16 a[48:51], v[6:9], v[14:17], a[48:51]
	v_mfma_f32_16x16x32_f16 a[52:55], v[6:9], v[18:21], a[52:55]
	s_waitcnt lgkmcnt(11)
	v_mfma_f32_16x16x32_f16 a[56:59], v[2:5], v[14:17], a[56:59]
	v_mfma_f32_16x16x32_f16 a[68:71], v[2:5], v[18:21], a[68:71]
	s_waitcnt lgkmcnt(8)
	v_mfma_f32_16x16x32_f16 a[0:3], v[70:73], v[82:85], a[0:3]
	ds_read_b128 v[14:17], v150
	v_mfma_f32_16x16x32_f16 a[4:7], v[70:73], v[86:89], a[4:7]
	ds_read_b128 v[18:21], v152
	s_waitcnt lgkmcnt(9)
	v_mfma_f32_16x16x32_f16 a[12:15], v[66:69], v[82:85], a[12:15]
	ds_read_b128 v[42:45], v168
	v_mfma_f32_16x16x32_f16 a[16:19], v[66:69], v[86:89], a[16:19]
	ds_read_b128 v[38:41], v168 offset:1024
	s_waitcnt lgkmcnt(10)
	v_mfma_f32_16x16x32_f16 a[28:31], v[58:61], v[82:85], a[28:31]
	ds_read_b128 v[34:37], v168 offset:2048
	v_mfma_f32_16x16x32_f16 a[60:63], v[58:61], v[86:89], a[60:63]
	ds_read_b128 v[30:33], v168 offset:3072
	s_waitcnt lgkmcnt(11)
	v_mfma_f32_16x16x32_f16 a[8:11], v[54:57], v[82:85], a[8:11]
	ds_read_b128 v[26:29], v168 offset:4096
	v_mfma_f32_16x16x32_f16 a[20:23], v[54:57], v[86:89], a[20:23]
	ds_read_b128 v[22:25], v168 offset:5120
	s_waitcnt lgkmcnt(12)
	v_mfma_f32_16x16x32_f16 a[24:27], v[46:49], v[82:85], a[24:27]
	ds_read_b128 v[10:13], v168 offset:6144
	v_mfma_f32_16x16x32_f16 a[36:39], v[46:49], v[86:89], a[36:39]
	ds_read_b128 v[6:9], v168 offset:7168
	s_waitcnt lgkmcnt(13)
	v_mfma_f32_16x16x32_f16 a[44:47], v[50:53], v[82:85], a[44:47]
	ds_read_b128 v[2:5], v168 offset:8192
	v_mfma_f32_16x16x32_f16 a[64:67], v[50:53], v[86:89], a[64:67]
	s_waitcnt lgkmcnt(13)
	v_mfma_f32_16x16x32_f16 a[32:35], v[62:65], v[82:85], a[32:35]
	v_mfma_f32_16x16x32_f16 a[40:43], v[62:65], v[86:89], a[40:43]
	s_waitcnt lgkmcnt(12)
	v_mfma_f32_16x16x32_f16 a[48:51], v[74:77], v[82:85], a[48:51]
	v_mfma_f32_16x16x32_f16 a[52:55], v[74:77], v[86:89], a[52:55]
	s_waitcnt lgkmcnt(11)
	v_mfma_f32_16x16x32_f16 a[56:59], v[78:81], v[82:85], a[56:59]
	v_mfma_f32_16x16x32_f16 a[68:71], v[78:81], v[86:89], a[68:71]
	s_waitcnt lgkmcnt(8)
	v_mfma_f32_16x16x32_f16 a[0:3], v[42:45], v[14:17], a[0:3]
	ds_read_b128 v[82:85], v151
	v_mfma_f32_16x16x32_f16 a[4:7], v[42:45], v[18:21], a[4:7]
	ds_read_b128 v[86:89], v153
	s_waitcnt lgkmcnt(9)
	v_mfma_f32_16x16x32_f16 a[12:15], v[38:41], v[14:17], a[12:15]
	ds_read_b128 v[70:73], v168 offset:9216
	v_mfma_f32_16x16x32_f16 a[16:19], v[38:41], v[18:21], a[16:19]
	ds_read_b128 v[66:69], v168 offset:10240
	s_waitcnt lgkmcnt(10)
	v_mfma_f32_16x16x32_f16 a[28:31], v[34:37], v[14:17], a[28:31]
	ds_read_b128 v[58:61], v168 offset:11264
	v_mfma_f32_16x16x32_f16 a[60:63], v[34:37], v[18:21], a[60:63]
	ds_read_b128 v[54:57], v168 offset:12288
	s_waitcnt lgkmcnt(11)
	v_mfma_f32_16x16x32_f16 a[8:11], v[30:33], v[14:17], a[8:11]
	ds_read_b128 v[46:49], v168 offset:13312
	v_mfma_f32_16x16x32_f16 a[20:23], v[30:33], v[18:21], a[20:23]
	ds_read_b128 v[50:53], v168 offset:14336
	s_waitcnt lgkmcnt(12)
	v_mfma_f32_16x16x32_f16 a[24:27], v[26:29], v[14:17], a[24:27]
	ds_read_b128 v[62:65], v168 offset:15360
	v_mfma_f32_16x16x32_f16 a[36:39], v[26:29], v[18:21], a[36:39]
	ds_read_b128 v[74:77], v168 offset:16384
	s_waitcnt lgkmcnt(13)
	v_mfma_f32_16x16x32_f16 a[44:47], v[22:25], v[14:17], a[44:47]
	ds_read_b128 v[78:81], v168 offset:17408
	v_mfma_f32_16x16x32_f16 a[64:67], v[22:25], v[18:21], a[64:67]
	s_waitcnt lgkmcnt(13)
	v_mfma_f32_16x16x32_f16 a[32:35], v[10:13], v[14:17], a[32:35]
	v_mfma_f32_16x16x32_f16 a[40:43], v[10:13], v[18:21], a[40:43]
	s_waitcnt lgkmcnt(12)
	v_mfma_f32_16x16x32_f16 a[48:51], v[6:9], v[14:17], a[48:51]
	v_mfma_f32_16x16x32_f16 a[52:55], v[6:9], v[18:21], a[52:55]
	s_waitcnt lgkmcnt(11)
	v_mfma_f32_16x16x32_f16 a[56:59], v[2:5], v[14:17], a[56:59]
	v_mfma_f32_16x16x32_f16 a[68:71], v[2:5], v[18:21], a[68:71]
	s_waitcnt vmcnt(5) lgkmcnt(0)
	s_barrier
	s_add_u32 s52, s50, 0x1f800
	s_addc_u32 s53, s51, 0
	s_add_i32 m0, s42, 0x1f000
	s_nop 0
	global_load_lds_dwordx4 v137, s[52:53]
	s_add_i32 m0, s43, 0x1f000
	s_nop 0
	global_load_lds_dwordx4 v138, s[52:53]
	s_cmp_lt_u32 s42, 0x800
	s_cbranch_scc0 .Lk4_st4_7
	s_add_i32 m0, s44, 0x1f000
	s_nop 0
	global_load_lds_dwordx4 v139, s[52:53]

.LBB3_32:
	s_barrier
	s_add_u32 s52, s10, 0x1000000
	s_addc_u32 s53, s11, 0
	v_add_u32_e32 v61, 0xe000, v90
	v_lshlrev_b32_e32 v62, 2, v96
	s_nop 0
	v_readfirstlane_b32 s44, v61
	s_mov_b32 m0, s44
	s_nop 0
	global_load_lds_dwordx4 v62, s[52:53] nt
	v_add_u32_e32 v61, 0xe000, v91
	v_lshlrev_b32_e32 v62, 2, v98
	s_nop 0
	v_readfirstlane_b32 s44, v61
	s_mov_b32 m0, s44
	s_nop 0
	global_load_lds_dwordx4 v62, s[52:53] nt
	v_add_u32_e32 v61, 0xe000, v119
	v_lshlrev_b32_e32 v62, 2, v100
	s_nop 0
	v_readfirstlane_b32 s44, v61
	s_mov_b32 m0, s44
	s_nop 0
	global_load_lds_dwordx4 v62, s[52:53] nt
	v_mbcnt_lo_u32_b32 v63, -1, 0
	v_mbcnt_hi_u32_b32 v63, -1, v63
	v_lshlrev_b32_e32 v63, 4, v63
	v_add_u32_e32 v64, v91, v63
	v_add_u32_e32 v65, v119, v63
	v_add_u32_e32 v66, v118, v63
	v_add_u32_e32 v67, v90, v63
	ds_write_b128 v64, v[128:131]
	ds_write_b128 v65, v[132:135]
	ds_write_b128 v66, v[172:175] offset:28672
	ds_write_b128 v67, v[176:179] offset:28672
	ds_write_b128 v64, v[140:143] offset:28672
	ds_write_b128 v65, v[144:147] offset:28672
	ds_write_b128 v66, v[124:127] offset:57344
	v_lshl_add_u32 v0, v120, 5, s22
	v_or_b32_e32 v1, s23, v121
	s_movk_i32 s0, 0x7f
	v_lshl_or_b32 v7, v93, 1, v0
	s_movk_i32 s1, 0x7e
	s_nop 15
	s_nop 15
	v_cmp_eq_u32_e64 s[4:5], s1, v7
	s_nop 7
	v_cmp_gt_u32_e32 vcc, s0, v1
	v_accvgpr_read_b32 v5, a14
	v_cmp_eq_u32_e64 s[0:1], 0, v1
	v_or_b32_e32 v4, v93, v7
	v_cmp_eq_u32_e64 s[2:3], 0, v4
	v_cndmask_b32_e64 v14, v5, 0, s[0:1]
	v_accvgpr_read_b32 v5, a13
	v_cndmask_b32_e64 v22, v5, 0, s[0:1]
	v_accvgpr_read_b32 v5, a12
	v_cndmask_b32_e64 v116, v5, 0, s[0:1]
	v_accvgpr_read_b32 v5, a49
	v_cndmask_b32_e32 v16, 0, v5, vcc
	v_accvgpr_read_b32 v5, a48
	v_cndmask_b32_e32 v28, 0, v5, vcc
	v_accvgpr_read_b32 v5, a30
	v_cndmask_b32_e64 v10, v5, 0, s[0:1]
	v_accvgpr_read_b32 v5, a29
	v_cndmask_b32_e64 v24, v5, 0, s[0:1]
	v_accvgpr_read_b32 v5, a28
	v_cndmask_b32_e64 v42, v5, 0, s[0:1]
	v_accvgpr_read_b32 v5, a57
	v_cndmask_b32_e32 v20, 0, v5, vcc
	v_accvgpr_read_b32 v5, a56
	v_cndmask_b32_e32 v38, 0, v5, vcc
	v_accvgpr_read_b32 v5, a6
	v_cndmask_b32_e64 v15, v5, 0, s[0:1]
	v_accvgpr_read_b32 v5, a5
	v_cndmask_b32_e64 v23, v5, 0, s[0:1]
	v_accvgpr_read_b32 v5, a4
	v_cndmask_b32_e64 v117, v5, 0, s[0:1]
	v_accvgpr_read_b32 v5, a41
	v_cndmask_b32_e32 v17, 0, v5, vcc
	v_accvgpr_read_b32 v5, a40
	v_cndmask_b32_e32 v29, 0, v5, vcc
	v_accvgpr_read_b32 v5, a17
	v_cndmask_b32_e64 v37, v5, 0, s[0:1]
	v_accvgpr_read_b32 v5, a16
	v_cndmask_b32_e64 v47, v5, 0, s[0:1]
	v_accvgpr_read_b32 v5, a52
	v_cndmask_b32_e32 v45, 0, v5, vcc
	v_accvgpr_read_b32 v5, a68
	v_cndmask_b32_e32 v12, 0, v5, vcc
	v_accvgpr_read_b32 v5, a0
	s_or_b64 s[8:9], s[2:3], s[0:1]
	v_cmp_eq_u32_e64 s[6:7], 15, v93
	v_accvgpr_read_b32 v11, a8
	v_cndmask_b32_e64 v112, v5, 0, s[8:9]
	v_accvgpr_read_b32 v4, a67
	v_mov_b32_e32 v5, 0x90
	s_and_b64 s[4:5], s[6:7], s[4:5]
	v_mov_b64_e32 v[40:41], v[16:17]
	v_cndmask_b32_e64 v16, v11, 0, s[2:3]
	v_cndmask_b32_e64 v11, 12, v5, s[6:7]
	v_cndmask_b32_e64 v61, v4, 0, s[4:5]
	v_accvgpr_read_b32 v4, a61
	s_or_b64 s[6:7], s[4:5], s[0:1]
	v_cndmask_b32_e64 v87, v4, 0, s[6:7]
	v_accvgpr_read_b32 v4, a60
	v_cndmask_b32_e64 v86, v4, 0, s[6:7]
	v_accvgpr_read_b32 v4, a65
	v_cndmask_b32_e64 v5, v4, 0, s[4:5]
	v_accvgpr_read_b32 v4, a64
	v_cndmask_b32_e64 v4, v4, 0, s[4:5]
	s_lshl_b32 s14, s18, 2
	v_mov_b64_e32 v[32:33], v[4:5]
	v_lshl_or_b32 v4, v122, 18, s14
	v_mov_b32_e32 v5, 0
	v_mov_b64_e32 v[62:63], v[14:15]
	v_lshl_add_u64 v[14:15], s[12:13], 0, v[4:5]
	v_lshlrev_b32_e32 v4, 7, v1
	v_lshl_add_u64 v[14:15], v[4:5], 2, v[14:15]
	v_lshlrev_b32_e32 v4, 2, v7
	v_mul_u32_u24_e32 v1, 24, v122
	v_lshl_add_u64 v[54:55], v[14:15], 0, v[4:5]
	v_mbcnt_lo_u32_b32 v138, -1, 0
	v_mbcnt_hi_u32_b32 v138, -1, v138
	v_and_b32_e32 v138, 1, v138
	v_mul_u32_u24_e32 v138, 0xfff8, v138
	v_add_u32_e32 v138, 0xffff0000, v138
	v_mov_b32_e32 v139, -1
	v_lshl_add_u64 v[134:135], v[54:55], 0, v[138:139]
	s_mov_b32 s28, 0x55555555
	s_mov_b32 s29, 0x55555555
	s_mov_b32 s30, 0xaaaaaaaa
	s_mov_b32 s31, 0xaaaaaaaa
	v_or_b32_e32 v1, v1, v121
	v_lshlrev_b32_e32 v4, 7, v120
	s_movk_i32 s12, 0x120
	v_mad_u32_u24 v1, v1, s12, v4
	s_add_u32 s12, s10, 0x800000
	v_accvgpr_read_b32 v7, a72
	v_mov_b64_e32 v[80:81], v[28:29]
	s_addc_u32 s13, s11, 0
	v_lshlrev_b64 v[28:29], 2, v[94:95]
	v_readfirstlane_b32 s14, v7
	v_add_u32_e32 v7, 0, v90
	v_lshl_add_u64 v[4:5], s[12:13], 0, v[28:29]
	s_mov_b32 m0, s14
	v_lshlrev_b64 v[30:31], 2, v[96:97]
	v_readfirstlane_b32 s14, v7
	v_mov_b32_e32 v14, v7
	v_add_u32_e32 v7, 0, v91
	s_waitcnt lgkmcnt(0)
	v_lshlrev_b64 v[56:57], 2, v[98:99]
	v_mov_b32_e32 v19, v7
	v_lshlrev_b64 v[58:59], 2, v[100:101]
	v_add_u32_e32 v7, 0, v119
	v_accvgpr_read_b32 v25, a72
	v_mov_b32_e32 v21, v7
	v_lshl_add_u32 v15, v93, 3, v1
	v_add_u32_e32 v1, v1, v11
	s_waitcnt vmcnt(16)
	v_accvgpr_write_b32 a12, v14
	v_mov_b64_e32 v[124:125], v[56:57]
	v_accvgpr_write_b32 a13, v19
	v_mov_b64_e32 v[126:127], v[58:59]
	v_accvgpr_write_b32 a16, v21
	s_waitcnt lgkmcnt(0)
	s_barrier
	v_add_u32_e32 v14, 0x16010, v15
	v_mov_b32_e32 v122, v15
	v_add_u32_e32 v15, 0x16000, v1
	ds_read_b64 v[64:65], v14
	ds_read_b64 v[66:67], v14 offset:288
	ds_read_b64 v[68:69], v14 offset:576
	ds_read_b64 v[76:77], v14 offset:1728
	ds_read_b64 v[78:79], v14 offset:2016
	ds_read_b64 v[4:5], v14 offset:2304
	ds_read_b64 v[84:85], v14 offset:3456
	ds_read_b64 v[74:75], v14 offset:3744
	ds_read_b64 v[88:89], v14 offset:4032
	ds_read_b64 v[100:101], v14 offset:5184
	ds_read_b64 v[106:107], v14 offset:5472
	ds_read_b64 v[120:121], v14 offset:5760
	ds_read_b32 v43, v15
	ds_read_b32 v19, v15 offset:288
	ds_read_b32 v39, v15 offset:576
	ds_read_b32 v25, v15 offset:1728
	ds_read_b32 v7, v15 offset:2016
	ds_read_b32 v21, v15 offset:2304
	ds_read_b32 v11, v15 offset:3456
	ds_read_b32 v35, v15 offset:3744
	ds_read_b32 v59, v15 offset:4032
	ds_read_b32 v57, v15 offset:5184
	ds_read_b32 v51, v15 offset:5472
	ds_read_b32 v49, v15 offset:5760
	s_waitcnt lgkmcnt(0)
	v_accvgpr_read_b32 v8, a26
	v_mov_b32_e32 v46, v43
	v_mov_b32_e32 v113, v65
	v_mov_b32_e32 v26, v19
	v_mov_b32_dpp v46, v65 row_shr:1 row_mask:0xf bank_mask:0xf
	v_pk_mul_f32 v[70:71], v[112:113], v[46:47]
	v_accvgpr_read_b32 v9, a22
	v_accvgpr_read_b32 v27, a36
	v_mov_b32_dpp v43, v64 row_shl:1 row_mask:0xf bank_mask:0xf
	v_mov_b32_dpp v26, v67 row_shr:1 row_mask:0xf bank_mask:0xf
	v_pk_fma_f32 v[70:71], v[64:65], v[116:117], v[70:71] op_sel_hi:[0,1,1]
	v_pk_mov_b32 v[64:65], v[64:65], v[86:87] op_sel:[1,0]
	v_mov_b32_e32 v17, v67
	v_mov_b64_e32 v[102:103], v[8:9]
	v_accvgpr_read_b32 v8, a25
	v_accvgpr_read_b32 v114, a24
	v_accvgpr_read_b32 v9, a21
	v_accvgpr_read_b32 v115, a20
	v_accvgpr_read_b32 v2, a32
	v_mov_b64_e32 v[82:83], v[30:31]
	v_pk_fma_f32 v[70:71], v[64:65], v[42:43], v[70:71]
	v_pk_mul_f32 v[64:65], v[16:17], v[26:27]
	v_mov_b64_e32 v[30:31], v[32:33]
	v_accvgpr_read_b32 v18, a44
	v_mov_b64_e32 v[104:105], v[8:9]
	v_cndmask_b32_e32 v9, 0, v2, vcc
	v_accvgpr_write_b32 a4, v14
	v_mov_b32_dpp v19, v66 row_shl:1 row_mask:0xf bank_mask:0xf
	v_pk_fma_f32 v[64:65], v[66:67], v[114:115], v[64:65] op_sel_hi:[0,1,1]
	v_pk_mov_b32 v[66:67], v[66:67], v[30:31] op_sel:[1,0]
	v_accvgpr_read_b32 v14, a69
	v_mov_b32_e32 v44, v39
	v_mov_b32_e32 v60, v1
	v_pk_fma_f32 v[66:67], v[66:67], v[18:19], v[64:65]
	v_cndmask_b32_e32 v14, 0, v14, vcc
	v_cndmask_b32_e64 v0, v9, 0, s[2:3]
	v_mov_b32_dpp v44, v69 row_shr:1 row_mask:0xf bank_mask:0xf
	v_pk_add_f32 v[70:71], v[70:71], 0 op_sel_hi:[1,0]
	v_mov_b32_e32 v1, v69
	v_accvgpr_write_b32 a0, v15
	v_cndmask_b32_e64 v15, v14, 0, s[4:5]
	v_cndmask_b32_e64 v14, v12, 0, s[4:5]
	v_pk_add_f32 v[66:67], v[70:71], v[66:67]
	v_pk_mul_f32 v[70:71], v[0:1], v[44:45]
	v_mov_b32_dpp v39, v68 row_shl:1 row_mask:0xf bank_mask:0xf
	v_pk_fma_f32 v[70:71], v[68:69], v[80:81], v[70:71] op_sel_hi:[0,1,1]
	v_pk_mov_b32 v[68:69], v[68:69], v[14:15] op_sel:[1,0]
	v_accvgpr_read_b32 v9, a1
	v_pk_fma_f32 v[68:69], v[68:69], v[38:39], v[70:71]
	v_mov_b32_e32 v36, v25
	v_cndmask_b32_e64 v64, v9, 0, s[8:9]
	v_pk_add_f32 v[66:67], v[66:67], v[68:69]
	v_mov_b32_dpp v36, v77 row_shr:1 row_mask:0xf bank_mask:0xf
	v_mov_b32_e32 v65, v77
	v_mov_b64_e32 v[108:109], v[22:23]
	v_accvgpr_read_b32 v9, a9
	v_mov_b32_e32 v128, v66
	v_mov_b32_e32 v129, v67
	v_mov_b32_e32 v12, v7
	v_pk_mul_f32 v[66:67], v[64:65], v[36:37]
	v_accvgpr_read_b32 v13, a37
	v_mov_b64_e32 v[72:73], v[28:29]
	v_cndmask_b32_e64 v28, v9, 0, s[2:3]
	v_mov_b32_dpp v25, v76 row_shl:1 row_mask:0xf bank_mask:0xf
	v_mov_b32_dpp v12, v79 row_shr:1 row_mask:0xf bank_mask:0xf
	v_pk_fma_f32 v[66:67], v[76:77], v[108:109], v[66:67] op_sel_hi:[0,1,1]
	v_mov_b32_e32 v76, v77
	v_mov_b32_e32 v77, v87
	v_mov_b32_e32 v29, v79
	v_pk_fma_f32 v[66:67], v[76:77], v[24:25], v[66:67]
	v_pk_mul_f32 v[76:77], v[28:29], v[12:13]
	v_accvgpr_read_b32 v6, a45
	v_accvgpr_read_b32 v2, a33
	v_mov_b32_dpp v7, v78 row_shl:1 row_mask:0xf bank_mask:0xf
	v_pk_fma_f32 v[76:77], v[78:79], v[104:105], v[76:77] op_sel_hi:[0,1,1]
	v_mov_b32_e32 v78, v79
	v_mov_b32_e32 v79, v31
	v_cndmask_b32_e32 v2, 0, v2, vcc
	v_accvgpr_read_b32 v50, a53
	v_pk_fma_f32 v[76:77], v[78:79], v[6:7], v[76:77]
	v_mov_b32_e32 v78, v21
	v_accvgpr_write_b32 a44, v80
	v_cndmask_b32_e32 v79, 0, v50, vcc
	v_cndmask_b32_e64 v52, v2, 0, s[2:3]
	v_mov_b32_dpp v78, v5 row_shr:1 row_mask:0xf bank_mask:0xf
	v_pk_add_f32 v[66:67], v[66:67], 0 op_sel_hi:[1,0]
	v_mov_b32_e32 v53, v5
	v_accvgpr_write_b32 a45, v81
	v_accvgpr_write_b32 a21, v15
	v_pk_add_f32 v[80:81], v[66:67], v[76:77]
	v_pk_mul_f32 v[66:67], v[52:53], v[78:79]
	v_accvgpr_write_b32 a24, v40
	v_accvgpr_read_b32 v2, a2
	v_mov_b32_dpp v21, v4 row_shl:1 row_mask:0xf bank_mask:0xf
	v_pk_fma_f32 v[66:67], v[4:5], v[40:41], v[66:67] op_sel_hi:[0,1,1]
	v_accvgpr_write_b32 a25, v41
	v_mov_b32_e32 v4, v5
	v_accvgpr_read_b32 v5, a21
	v_cndmask_b32_e64 v40, v2, 0, s[8:9]
	v_accvgpr_read_b32 v2, a62
	v_accvgpr_read_b32 v8, a18
	v_accvgpr_read_b32 v48, a63
	v_accvgpr_write_b32 a20, v14
	v_accvgpr_write_b32 a41, v23
	v_pk_fma_f32 v[4:5], v[4:5], v[20:21], v[66:67]
	s_mov_b64 s[12:13], 0x10000
	v_cndmask_b32_e64 v14, v2, 0, s[6:7]
	v_mov_b32_e32 v76, v11
	v_accvgpr_read_b32 v2, a10
	v_accvgpr_write_b32 a40, v22
	v_cndmask_b32_e64 v15, v48, 0, s[6:7]
	v_cndmask_b32_e64 v77, v8, 0, s[0:1]
	v_pk_add_f32 v[4:5], v[80:81], v[4:5]
	v_lshl_add_u64 v[136:137], v[134:135], 0, s[12:13]
	v_mov_b32_dpp v76, v85 row_shr:1 row_mask:0xf bank_mask:0xf
	v_mov_b32_e32 v41, v85
	v_cndmask_b32_e64 v22, v2, 0, s[2:3]
	v_mov_b32_e32 v2, v35
	v_accvgpr_read_b32 v1, a50
	v_accvgpr_read_b32 v3, a38
	s_mov_b64 s[32:33], vcc
	s_nop 1
	s_mov_b64 vcc, s[28:29]
	s_nop 0
	v_cndmask_b32_dpp v130, v4, v128, vcc quad_perm:[1,0,3,2] row_mask:0xf bank_mask:0xf
	v_cndmask_b32_dpp v131, v5, v129, vcc quad_perm:[1,0,3,2] row_mask:0xf bank_mask:0xf
	s_mov_b64 vcc, s[30:31]
	s_nop 0
	v_cndmask_b32_dpp v132, v128, v4, vcc quad_perm:[1,0,3,2] row_mask:0xf bank_mask:0xf
	v_cndmask_b32_dpp v133, v129, v5, vcc quad_perm:[1,0,3,2] row_mask:0xf bank_mask:0xf
	global_store_dwordx4 v[136:137], v[130:133], off sc0 sc1 nt
	s_nop 1
	s_mov_b64 vcc, s[32:33]
	v_mov_b64_e32 v[8:9], v[14:15]
	v_pk_mul_f32 v[4:5], v[40:41], v[76:77]
	v_mov_b64_e32 v[66:67], v[62:63]
	v_mov_b32_dpp v2, v75 row_shr:1 row_mask:0xf bank_mask:0xf
	v_mov_b32_e32 v23, v75
	v_cndmask_b32_e32 v62, 0, v1, vcc
	v_accvgpr_read_b32 v1, a42
	v_mov_b32_dpp v11, v84 row_shl:1 row_mask:0xf bank_mask:0xf
	v_pk_fma_f32 v[4:5], v[84:85], v[66:67], v[4:5] op_sel_hi:[0,1,1]
	v_pk_mov_b32 v[80:81], v[84:85], v[8:9] op_sel:[1,0]
	v_pk_mul_f32 v[84:85], v[22:23], v[2:3]
	v_accvgpr_read_b32 v2, a58
	v_cndmask_b32_e32 v63, 0, v1, vcc
	v_accvgpr_read_b32 v1, a70
	v_pk_fma_f32 v[80:81], v[80:81], v[10:11], v[4:5]
	v_accvgpr_read_b32 v4, a66
	v_cndmask_b32_e32 v58, 0, v2, vcc
	v_cndmask_b32_e32 v1, 0, v1, vcc
	v_accvgpr_read_b32 v2, a71
	v_cndmask_b32_e64 v8, v4, 0, s[4:5]
	v_cndmask_b32_e32 v2, 0, v2, vcc
	v_cndmask_b32_e64 v4, v1, 0, s[4:5]
	v_accvgpr_read_b32 v1, a34
	v_mov_b32_e32 v9, v61
	v_cndmask_b32_e64 v5, v2, 0, s[4:5]
	v_cndmask_b32_e32 v1, 0, v1, vcc
	v_accvgpr_read_b32 v2, a54
	v_mov_b32_e32 v92, v59
	v_accvgpr_read_b32 v34, a46
	v_mov_b32_dpp v35, v74 row_shl:1 row_mask:0xf bank_mask:0xf
	v_pk_fma_f32 v[84:85], v[74:75], v[102:103], v[84:85] op_sel_hi:[0,1,1]
	v_pk_mov_b32 v[74:75], v[74:75], v[8:9] op_sel:[1,0]
	v_cndmask_b32_e32 v93, 0, v2, vcc
	v_mov_b32_dpp v92, v89 row_shr:1 row_mask:0xf bank_mask:0xf
	v_cndmask_b32_e64 v96, v1, 0, s[2:3]
	v_mov_b32_e32 v97, v89
	v_accvgpr_read_b32 v1, a31
	v_pk_fma_f32 v[74:75], v[74:75], v[34:35], v[84:85]
	v_pk_mul_f32 v[84:85], v[96:97], v[92:93]
	v_accvgpr_write_b32 a8, v62
	v_cndmask_b32_e64 v56, v1, 0, s[0:1]
	v_accvgpr_read_b32 v1, a15
	v_pk_fma_f32 v[84:85], v[88:89], v[62:63], v[84:85] op_sel_hi:[0,1,1]
	v_accvgpr_write_b32 a9, v63
	v_cndmask_b32_e64 v62, v1, 0, s[0:1]
	v_accvgpr_read_b32 v1, a7
	v_cndmask_b32_e64 v63, v1, 0, s[0:1]
	v_accvgpr_read_b32 v1, a19
	v_pk_add_f32 v[80:81], v[80:81], 0 op_sel_hi:[1,0]
	v_mov_b32_dpp v59, v88 row_shl:1 row_mask:0xf bank_mask:0xf
	v_pk_mov_b32 v[88:89], v[88:89], v[4:5] op_sel:[1,0]
	v_cndmask_b32_e64 v95, v1, 0, s[0:1]
	v_accvgpr_read_b32 v1, a3
	v_accvgpr_write_b32 a36, v104
	v_pk_add_f32 v[80:81], v[80:81], v[74:75]
	v_pk_fma_f32 v[84:85], v[88:89], v[58:59], v[84:85]
	v_mov_b32_e32 v94, v57
	v_cndmask_b32_e64 v98, v1, 0, s[8:9]
	v_accvgpr_read_b32 v1, a11
	v_accvgpr_write_b32 a37, v105
	v_accvgpr_write_b32 a32, v102
	v_pk_add_f32 v[80:81], v[80:81], v[84:85]
	s_mov_b64 s[4:5], 0x20000
	v_mov_b32_dpp v94, v101 row_shr:1 row_mask:0xf bank_mask:0xf
	v_mov_b32_e32 v99, v101
	v_cndmask_b32_e64 v104, v1, 0, s[2:3]
	v_accvgpr_read_b32 v1, a59
	v_accvgpr_write_b32 a29, v15
	v_accvgpr_write_b32 a33, v103
	v_accvgpr_write_b32 a49, v5
	v_lshl_add_u64 v[84:85], v[54:55], 0, s[4:5]
	v_mov_b32_e32 v128, v80
	v_mov_b32_e32 v129, v81
	v_pk_mul_f32 v[80:81], v[98:99], v[94:95]
	v_mov_b32_e32 v102, v51
	v_cndmask_b32_e32 v48, 0, v1, vcc
	v_accvgpr_read_b32 v1, a51
	v_accvgpr_write_b32 a48, v4
	v_mov_b32_dpp v57, v100 row_shl:1 row_mask:0xf bank_mask:0xf
	v_pk_fma_f32 v[80:81], v[100:101], v[62:63], v[80:81] op_sel_hi:[0,1,1]
	v_mov_b32_e32 v84, v101
	v_accvgpr_read_b32 v85, a29
	v_accvgpr_read_b32 v103, a39
	v_mov_b32_dpp v102, v107 row_shr:1 row_mask:0xf bank_mask:0xf
	v_mov_b32_e32 v105, v107
	v_cndmask_b32_e32 v4, 0, v1, vcc
	v_accvgpr_read_b32 v1, a43
	v_pk_fma_f32 v[80:81], v[84:85], v[56:57], v[80:81]
	v_accvgpr_read_b32 v30, a27
	v_accvgpr_read_b32 v31, a23
	v_pk_mul_f32 v[84:85], v[104:105], v[102:103]
	v_cndmask_b32_e32 v5, 0, v1, vcc
	v_accvgpr_read_b32 v1, a35
	v_accvgpr_read_b32 v50, a47
	v_mov_b32_dpp v51, v106 row_shl:1 row_mask:0xf bank_mask:0xf
	v_pk_fma_f32 v[84:85], v[106:107], v[30:31], v[84:85] op_sel_hi:[0,1,1]
	v_mov_b32_e32 v106, v107
	v_mov_b32_e32 v107, v9
	v_cndmask_b32_e32 v1, 0, v1, vcc
	v_accvgpr_read_b32 v2, a55
	v_mov_b32_e32 v108, v49
	v_pk_fma_f32 v[84:85], v[106:107], v[50:51], v[84:85]
	v_pk_add_f32 v[80:81], v[80:81], 0 op_sel_hi:[1,0]
	v_cndmask_b32_e32 v109, 0, v2, vcc
	v_mov_b32_dpp v108, v121 row_shr:1 row_mask:0xf bank_mask:0xf
	v_cndmask_b32_e64 v110, v1, 0, s[2:3]
	v_mov_b32_e32 v111, v121
	v_pk_add_f32 v[80:81], v[80:81], v[84:85]
	v_pk_mul_f32 v[84:85], v[110:111], v[108:109]
	v_mov_b32_dpp v49, v120 row_shl:1 row_mask:0xf bank_mask:0xf
	v_pk_fma_f32 v[84:85], v[120:121], v[4:5], v[84:85] op_sel_hi:[0,1,1]
	v_mov_b32_e32 v120, v121
	v_accvgpr_read_b32 v121, a49
	v_pk_fma_f32 v[84:85], v[120:121], v[48:49], v[84:85]
	s_mov_b64 s[0:1], 0x30000
	v_pk_add_f32 v[80:81], v[80:81], v[84:85]
	v_lshl_add_u64 v[136:137], v[134:135], 0, s[0:1]
	v_add_u32_e32 v1, s17, v118
	s_add_u32 s0, s10, 0x1400000
	s_mov_b64 s[32:33], vcc
	s_nop 1
	s_mov_b64 vcc, s[28:29]
	s_nop 0
	v_cndmask_b32_dpp v130, v80, v128, vcc quad_perm:[1,0,3,2] row_mask:0xf bank_mask:0xf
	v_cndmask_b32_dpp v131, v81, v129, vcc quad_perm:[1,0,3,2] row_mask:0xf bank_mask:0xf
	s_mov_b64 vcc, s[30:31]
	s_nop 0
	v_cndmask_b32_dpp v132, v128, v80, vcc quad_perm:[1,0,3,2] row_mask:0xf bank_mask:0xf
	v_cndmask_b32_dpp v133, v129, v81, vcc quad_perm:[1,0,3,2] row_mask:0xf bank_mask:0xf
	global_store_dwordx4 v[136:137], v[130:133], off sc0 sc1 nt
	s_nop 1
	s_mov_b64 vcc, s[32:33]
	v_readfirstlane_b32 s2, v1
	s_addc_u32 s1, s11, 0
	v_add_u32_e32 v1, s17, v90
	s_waitcnt vmcnt(5)
	v_lshl_add_u64 v[80:81], s[0:1], 0, v[72:73]
	s_mov_b32 m0, s2
	v_readfirstlane_b32 s2, v1
	v_mov_b64_e32 v[74:75], v[82:83]
	v_add_u32_e32 v1, s17, v91
	s_waitcnt lgkmcnt(0)
	s_barrier
	global_load_lds_dwordx4 v[80:81], off nt
	v_lshl_add_u64 v[80:81], s[0:1], 0, v[74:75]
	s_mov_b32 m0, s2
	v_readfirstlane_b32 s2, v1
	v_add_u32_e32 v1, s17, v119
	global_load_lds_dwordx4 v[80:81], off nt
	v_lshl_add_u64 v[80:81], s[0:1], 0, v[124:125]
	s_mov_b32 m0, s2
	v_readfirstlane_b32 s2, v1
	global_load_lds_dwordx4 v[80:81], off nt
	v_lshl_add_u64 v[80:81], s[0:1], 0, v[126:127]
	s_mov_b32 m0, s2
	v_accvgpr_write_b32 a53, v33
	v_accvgpr_write_b32 a2, v62
	v_accvgpr_write_b32 a7, v5
	v_accvgpr_write_b32 a22, v124
	v_accvgpr_write_b32 a30, v126
	global_load_lds_dwordx4 v[80:81], off nt
	v_accvgpr_write_b32 a52, v32
	v_accvgpr_write_b32 a3, v63
	v_accvgpr_write_b32 a6, v4
	v_mov_b64_e32 v[32:33], v[72:73]
	v_accvgpr_write_b32 a23, v125
	v_accvgpr_write_b32 a31, v127
	v_add_u32_e32 v2, 0x1d010, v122
	v_accvgpr_write_b32 a10, v122
	v_add_u32_e32 v5, 0x1d000, v60
	v_mov_b32_e32 v4, v60
	ds_read_b64 v[62:63], v2
	ds_read_b64 v[60:61], v2 offset:288
	ds_read_b64 v[72:73], v2 offset:576
	ds_read_b64 v[70:71], v2 offset:1728
	ds_read_b64 v[68:69], v2 offset:2016
	ds_read_b64 v[82:83], v2 offset:2304
	ds_read_b64 v[80:81], v2 offset:3456
	ds_read_b64 v[84:85], v2 offset:3744
	ds_read_b64 v[126:127], v2 offset:4032
	ds_read_b64 v[124:125], v2 offset:5184
	ds_read_b64 v[122:123], v2 offset:5472
	ds_read_b64 v[120:121], v2 offset:5760
	ds_read_b32 v43, v5
	ds_read_b32 v19, v5 offset:288
	ds_read_b32 v39, v5 offset:576
	ds_read_b32 v25, v5 offset:1728
	ds_read_b32 v7, v5 offset:2016
	ds_read_b32 v21, v5 offset:2304
	ds_read_b32 v11, v5 offset:3456
	ds_read_b32 v35, v5 offset:3744
	ds_read_b32 v59, v5 offset:4032
	ds_read_b32 v57, v5 offset:5184
	ds_read_b32 v51, v5 offset:5472
	ds_read_b32 v49, v5 offset:5760
	s_waitcnt lgkmcnt(0)
	v_mov_b64_e32 v[100:101], v[86:87]
	v_mov_b32_e32 v46, v43
	v_mov_b32_e32 v113, v63
	v_mov_b32_e32 v26, v19
	v_mov_b32_dpp v46, v63 row_shr:1 row_mask:0xf bank_mask:0xf
	v_pk_mul_f32 v[88:89], v[112:113], v[46:47]
	v_mov_b32_dpp v43, v62 row_shl:1 row_mask:0xf bank_mask:0xf
	v_pk_fma_f32 v[88:89], v[62:63], v[116:117], v[88:89] op_sel_hi:[0,1,1]
	v_pk_mov_b32 v[62:63], v[62:63], v[100:101] op_sel:[1,0]
	v_mov_b32_dpp v26, v61 row_shr:1 row_mask:0xf bank_mask:0xf
	v_mov_b32_e32 v17, v61
	v_pk_fma_f32 v[62:63], v[62:63], v[42:43], v[88:89]
	v_pk_mul_f32 v[88:89], v[16:17], v[26:27]
	v_accvgpr_write_b32 a34, v16
	v_accvgpr_read_b32 v16, a52
	v_accvgpr_read_b32 v17, a53
	v_mov_b32_dpp v19, v60 row_shl:1 row_mask:0xf bank_mask:0xf
	v_pk_fma_f32 v[88:89], v[60:61], v[114:115], v[88:89] op_sel_hi:[0,1,1]
	v_pk_mov_b32 v[60:61], v[60:61], v[16:17] op_sel:[1,0]
	v_mov_b32_e32 v44, v39
	v_accvgpr_write_b32 a28, v14
	v_pk_fma_f32 v[60:61], v[60:61], v[18:19], v[88:89]
	v_pk_add_f32 v[62:63], v[62:63], 0 op_sel_hi:[1,0]
	v_mov_b32_dpp v44, v73 row_shr:1 row_mask:0xf bank_mask:0xf
	v_mov_b32_e32 v1, v73
	v_accvgpr_read_b32 v14, a44
	v_accvgpr_read_b32 v89, a21
	v_pk_add_f32 v[60:61], v[62:63], v[60:61]
	v_pk_mul_f32 v[62:63], v[0:1], v[44:45]
	v_accvgpr_read_b32 v15, a45
	v_accvgpr_read_b32 v88, a20
	v_mov_b32_dpp v39, v72 row_shl:1 row_mask:0xf bank_mask:0xf
	v_pk_fma_f32 v[62:63], v[72:73], v[14:15], v[62:63] op_sel_hi:[0,1,1]
	v_pk_mov_b32 v[72:73], v[72:73], v[88:89] op_sel:[1,0]
	v_mov_b32_e32 v36, v25
	v_pk_fma_f32 v[62:63], v[72:73], v[38:39], v[62:63]
	s_mov_b64 s[0:1], 0x400000
	v_pk_add_f32 v[60:61], v[60:61], v[62:63]
	v_mov_b32_dpp v36, v71 row_shr:1 row_mask:0xf bank_mask:0xf
	v_mov_b32_e32 v65, v71
	v_accvgpr_read_b32 v87, a41
	v_lshl_add_u64 v[62:63], v[54:55], 0, s[0:1]
	v_mov_b32_e32 v128, v60
	v_mov_b32_e32 v129, v61
	v_pk_mul_f32 v[60:61], v[64:65], v[36:37]
	v_accvgpr_read_b32 v86, a40
	v_mov_b32_e32 v12, v7
	v_mov_b32_dpp v25, v70 row_shl:1 row_mask:0xf bank_mask:0xf
	v_pk_fma_f32 v[60:61], v[70:71], v[86:87], v[60:61] op_sel_hi:[0,1,1]
	v_mov_b32_e32 v62, v71
	v_mov_b32_e32 v63, v101
	v_mov_b32_dpp v12, v69 row_shr:1 row_mask:0xf bank_mask:0xf
	v_mov_b32_e32 v29, v69
	v_accvgpr_read_b32 v107, a37
	v_pk_fma_f32 v[60:61], v[62:63], v[24:25], v[60:61]
	v_pk_mul_f32 v[62:63], v[28:29], v[12:13]
	v_accvgpr_read_b32 v106, a36
	v_mov_b32_dpp v7, v68 row_shl:1 row_mask:0xf bank_mask:0xf
	v_pk_fma_f32 v[62:63], v[68:69], v[106:107], v[62:63] op_sel_hi:[0,1,1]
	v_mov_b32_e32 v68, v69
	v_mov_b32_e32 v69, v17
	v_mov_b32_e32 v78, v21
	v_pk_fma_f32 v[62:63], v[68:69], v[6:7], v[62:63]
	v_pk_add_f32 v[60:61], v[60:61], 0 op_sel_hi:[1,0]
	v_mov_b32_dpp v78, v83 row_shr:1 row_mask:0xf bank_mask:0xf
	v_mov_b32_e32 v53, v83
	v_accvgpr_read_b32 v14, a24
	v_pk_add_f32 v[60:61], v[60:61], v[62:63]
	v_pk_mul_f32 v[62:63], v[52:53], v[78:79]
	v_accvgpr_read_b32 v15, a25
	v_mov_b32_dpp v21, v82 row_shl:1 row_mask:0xf bank_mask:0xf
	v_pk_fma_f32 v[62:63], v[82:83], v[14:15], v[62:63] op_sel_hi:[0,1,1]
	v_mov_b32_e32 v68, v83
	v_mov_b32_e32 v69, v89
	v_pk_fma_f32 v[62:63], v[68:69], v[20:21], v[62:63]
	v_mov_b32_e32 v76, v11
	v_pk_add_f32 v[60:61], v[60:61], v[62:63]
	s_mov_b64 s[0:1], 0x410000
	v_mov_b32_dpp v76, v81 row_shr:1 row_mask:0xf bank_mask:0xf
	v_mov_b32_e32 v41, v81
	v_lshl_add_u64 v[136:137], v[134:135], 0, s[0:1]
	s_nop 1
	s_mov_b64 vcc, s[28:29]
	s_nop 0
	v_cndmask_b32_dpp v130, v60, v128, vcc quad_perm:[1,0,3,2] row_mask:0xf bank_mask:0xf
	v_cndmask_b32_dpp v131, v61, v129, vcc quad_perm:[1,0,3,2] row_mask:0xf bank_mask:0xf
	s_mov_b64 vcc, s[30:31]
	s_nop 0
	v_cndmask_b32_dpp v132, v128, v60, vcc quad_perm:[1,0,3,2] row_mask:0xf bank_mask:0xf
	v_cndmask_b32_dpp v133, v129, v61, vcc quad_perm:[1,0,3,2] row_mask:0xf bank_mask:0xf
	global_store_dwordx4 v[136:137], v[130:133], off sc0 sc1 nt
	s_nop 1
	v_pk_mul_f32 v[60:61], v[40:41], v[76:77]
	v_accvgpr_write_b32 a36, v66
	v_pk_fma_f32 v[60:61], v[80:81], v[66:67], v[60:61] op_sel_hi:[0,1,1]
	v_accvgpr_write_b32 a37, v67
	v_accvgpr_read_b32 v67, a29
	v_accvgpr_write_b32 a5, v2
	v_accvgpr_write_b32 a38, v100
	v_accvgpr_read_b32 v66, a28
	v_mov_b32_e32 v2, v35
	v_accvgpr_write_b32 a39, v101
	v_mov_b32_dpp v11, v80 row_shl:1 row_mask:0xf bank_mask:0xf
	v_pk_mov_b32 v[62:63], v[80:81], v[66:67] op_sel:[1,0]
	v_mov_b32_dpp v2, v85 row_shr:1 row_mask:0xf bank_mask:0xf
	v_mov_b32_e32 v23, v85
	v_accvgpr_read_b32 v101, a33
	v_pk_fma_f32 v[60:61], v[62:63], v[10:11], v[60:61]
	v_pk_mul_f32 v[62:63], v[22:23], v[2:3]
	v_accvgpr_read_b32 v100, a32
	v_mov_b32_dpp v35, v84 row_shl:1 row_mask:0xf bank_mask:0xf
	v_pk_fma_f32 v[62:63], v[84:85], v[100:101], v[62:63] op_sel_hi:[0,1,1]
	v_pk_mov_b32 v[68:69], v[84:85], v[8:9] op_sel:[1,0]
	v_mov_b32_e32 v92, v59
	v_pk_fma_f32 v[62:63], v[68:69], v[34:35], v[62:63]
	v_pk_add_f32 v[60:61], v[60:61], 0 op_sel_hi:[1,0]
	v_mov_b32_dpp v92, v127 row_shr:1 row_mask:0xf bank_mask:0xf
	v_mov_b32_e32 v97, v127
	v_accvgpr_read_b32 v17, a9
	v_accvgpr_read_b32 v71, a49
	v_pk_add_f32 v[60:61], v[60:61], v[62:63]
	v_pk_mul_f32 v[62:63], v[96:97], v[92:93]
	v_accvgpr_read_b32 v16, a8
	v_accvgpr_read_b32 v70, a48
	v_mov_b32_dpp v59, v126 row_shl:1 row_mask:0xf bank_mask:0xf
	v_pk_fma_f32 v[62:63], v[126:127], v[16:17], v[62:63] op_sel_hi:[0,1,1]
	v_pk_mov_b32 v[68:69], v[126:127], v[70:71] op_sel:[1,0]
	v_mov_b32_e32 v94, v57
	v_pk_fma_f32 v[62:63], v[68:69], v[58:59], v[62:63]
	v_accvgpr_write_b32 a20, v28
	v_pk_add_f32 v[60:61], v[60:61], v[62:63]
	s_mov_b64 s[0:1], 0x420000
	v_mov_b32_dpp v94, v125 row_shr:1 row_mask:0xf bank_mask:0xf
	v_mov_b32_e32 v99, v125
	v_accvgpr_read_b32 v29, a3
	v_lshl_add_u64 v[62:63], v[54:55], 0, s[0:1]
	v_mov_b32_e32 v128, v60
	v_mov_b32_e32 v129, v61
	v_pk_mul_f32 v[60:61], v[98:99], v[94:95]
	v_accvgpr_read_b32 v28, a2
	v_mov_b32_e32 v102, v51
	v_mov_b32_dpp v57, v124 row_shl:1 row_mask:0xf bank_mask:0xf
	v_pk_fma_f32 v[60:61], v[124:125], v[28:29], v[60:61] op_sel_hi:[0,1,1]
	v_mov_b32_e32 v62, v125
	v_mov_b32_e32 v63, v67
	v_mov_b32_dpp v102, v123 row_shr:1 row_mask:0xf bank_mask:0xf
	v_mov_b32_e32 v105, v123
	v_pk_fma_f32 v[60:61], v[62:63], v[56:57], v[60:61]
	v_pk_mul_f32 v[62:63], v[104:105], v[102:103]
	v_mov_b32_dpp v51, v122 row_shl:1 row_mask:0xf bank_mask:0xf
	v_pk_fma_f32 v[62:63], v[122:123], v[30:31], v[62:63] op_sel_hi:[0,1,1]
	v_accvgpr_write_b32 a28, v30
	v_mov_b32_e32 v68, v123
	v_mov_b32_e32 v69, v9
	v_mov_b32_e32 v108, v49
	v_accvgpr_write_b32 a29, v31
	v_pk_fma_f32 v[62:63], v[68:69], v[50:51], v[62:63]
	v_pk_add_f32 v[60:61], v[60:61], 0 op_sel_hi:[1,0]
	v_mov_b32_dpp v108, v121 row_shr:1 row_mask:0xf bank_mask:0xf
	v_mov_b32_e32 v111, v121
	v_accvgpr_read_b32 v31, a7
	v_pk_add_f32 v[60:61], v[60:61], v[62:63]
	v_pk_mul_f32 v[62:63], v[110:111], v[108:109]
	v_accvgpr_read_b32 v30, a6
	v_mov_b32_dpp v49, v120 row_shl:1 row_mask:0xf bank_mask:0xf
	v_pk_fma_f32 v[62:63], v[120:121], v[30:31], v[62:63] op_sel_hi:[0,1,1]
	v_mov_b32_e32 v68, v121
	v_mov_b32_e32 v69, v71
	v_pk_fma_f32 v[62:63], v[68:69], v[48:49], v[62:63]
	s_mov_b64 s[0:1], 0x430000
	v_pk_add_f32 v[60:61], v[60:61], v[62:63]
	v_lshl_add_u64 v[136:137], v[134:135], 0, s[0:1]
	v_add_u32_e32 v1, s16, v118
	s_add_u32 s0, s10, 0x1800000
	v_accvgpr_write_b32 a26, v114
	s_nop 1
	s_mov_b64 vcc, s[28:29]
	s_nop 0
	v_cndmask_b32_dpp v130, v60, v128, vcc quad_perm:[1,0,3,2] row_mask:0xf bank_mask:0xf
	v_cndmask_b32_dpp v131, v61, v129, vcc quad_perm:[1,0,3,2] row_mask:0xf bank_mask:0xf
	s_mov_b64 vcc, s[30:31]
	s_nop 0
	v_cndmask_b32_dpp v132, v128, v60, vcc quad_perm:[1,0,3,2] row_mask:0xf bank_mask:0xf
	v_cndmask_b32_dpp v133, v129, v61, vcc quad_perm:[1,0,3,2] row_mask:0xf bank_mask:0xf
	global_store_dwordx4 v[136:137], v[130:133], off sc0 sc1 nt
	s_nop 1
	v_readfirstlane_b32 s2, v1
	s_addc_u32 s1, s11, 0
	v_add_u32_e32 v1, s16, v90
	v_accvgpr_write_b32 a18, v116
	v_accvgpr_write_b32 a27, v115
	s_waitcnt vmcnt(16)
	v_lshl_add_u64 v[60:61], s[0:1], 0, v[32:33]
	s_mov_b32 m0, s2
	v_readfirstlane_b32 s2, v1
	v_add_u32_e32 v1, s16, v91
	v_accvgpr_read_b32 v115, a23
	v_accvgpr_write_b32 a19, v117
	s_waitcnt lgkmcnt(0)
	s_barrier
	global_load_lds_dwordx4 v[60:61], off nt
	v_lshl_add_u64 v[60:61], s[0:1], 0, v[74:75]
	s_mov_b32 m0, s2
	v_readfirstlane_b32 s2, v1
	v_accvgpr_read_b32 v114, a22
	v_add_u32_e32 v1, s16, v119
	v_accvgpr_read_b32 v117, a31
	global_load_lds_dwordx4 v[60:61], off nt
	v_lshl_add_u64 v[60:61], s[0:1], 0, v[114:115]
	s_mov_b32 m0, s2
	v_readfirstlane_b32 s2, v1
	v_accvgpr_read_b32 v116, a30
	global_load_lds_dwordx4 v[60:61], off nt
	v_lshl_add_u64 v[60:61], s[0:1], 0, v[116:117]
	s_mov_b32 m0, s2
	v_accvgpr_write_b32 a1, v5
	global_load_lds_dwordx4 v[60:61], off nt
	v_accvgpr_read_b32 v5, a10
	v_add_u32_e32 v2, 16, v5
	ds_read_b64 v[60:61], v2
	ds_read_b64 v[62:63], v2 offset:288
	ds_read_b64 v[68:69], v2 offset:576
	ds_read_b64 v[70:71], v2 offset:1728
	ds_read_b64 v[72:73], v2 offset:2016
	ds_read_b64 v[82:83], v2 offset:2304
	ds_read_b64 v[80:81], v2 offset:3456
	ds_read_b64 v[84:85], v2 offset:3744
	ds_read_b64 v[124:125], v2 offset:4032
	ds_read_b64 v[122:123], v2 offset:5184
	ds_read_b64 v[120:121], v2 offset:5472
	ds_read_b64 v[90:91], v2 offset:5760
	ds_read_b32 v43, v4
	ds_read_b32 v19, v4 offset:288
	ds_read_b32 v39, v4 offset:576
	ds_read_b32 v25, v4 offset:1728
	ds_read_b32 v7, v4 offset:2016
	ds_read_b32 v21, v4 offset:2304
	ds_read_b32 v11, v4 offset:3456
	ds_read_b32 v35, v4 offset:3744
	ds_read_b32 v59, v4 offset:4032
	ds_read_b32 v57, v4 offset:5184
	ds_read_b32 v51, v4 offset:5472
	ds_read_b32 v49, v4 offset:5760
	s_waitcnt lgkmcnt(0)
	v_accvgpr_write_b32 a46, v88
	v_mov_b32_e32 v46, v43
	v_accvgpr_write_b32 a8, v8
	v_mov_b32_e32 v113, v61
	v_mov_b32_dpp v46, v61 row_shr:1 row_mask:0xf bank_mask:0xf
	v_accvgpr_mov_b32 a42, a52
	v_accvgpr_write_b32 a47, v89
	v_accvgpr_write_b32 a9, v9
	v_pk_mul_f32 v[88:89], v[112:113], v[46:47]
	v_accvgpr_write_b32 a40, v112
	v_accvgpr_read_b32 v8, a18
	v_accvgpr_read_b32 v113, a39
	v_accvgpr_mov_b32 a43, a53
	v_accvgpr_write_b32 a51, v33
	v_accvgpr_write_b32 a52, v74
	v_accvgpr_read_b32 v9, a19
	v_accvgpr_read_b32 v112, a38
	v_mov_b32_e32 v26, v19
	v_accvgpr_write_b32 a50, v32
	v_accvgpr_write_b32 a53, v75
	v_mov_b32_dpp v43, v60 row_shl:1 row_mask:0xf bank_mask:0xf
	v_pk_fma_f32 v[88:89], v[60:61], v[8:9], v[88:89] op_sel_hi:[0,1,1]
	v_pk_mov_b32 v[60:61], v[60:61], v[112:113] op_sel:[1,0]
	v_mov_b32_dpp v26, v63 row_shr:1 row_mask:0xf bank_mask:0xf
	v_accvgpr_read_b32 v32, a34
	v_mov_b32_e32 v33, v63
	v_accvgpr_read_b32 v127, a27
	v_accvgpr_read_b32 v75, a43
	v_pk_fma_f32 v[60:61], v[60:61], v[42:43], v[88:89]
	v_pk_mul_f32 v[88:89], v[32:33], v[26:27]
	v_accvgpr_read_b32 v126, a26
	v_accvgpr_read_b32 v74, a42
	v_mov_b32_dpp v19, v62 row_shl:1 row_mask:0xf bank_mask:0xf
	v_pk_fma_f32 v[88:89], v[62:63], v[126:127], v[88:89] op_sel_hi:[0,1,1]
	v_pk_mov_b32 v[62:63], v[62:63], v[74:75] op_sel:[1,0]
	v_mov_b32_e32 v44, v39
	v_accvgpr_mov_b32 a14, a48
	v_pk_fma_f32 v[62:63], v[62:63], v[18:19], v[88:89]
	v_pk_add_f32 v[60:61], v[60:61], 0 op_sel_hi:[1,0]
	v_mov_b32_dpp v44, v69 row_shr:1 row_mask:0xf bank_mask:0xf
	v_mov_b32_e32 v1, v69
	v_accvgpr_mov_b32 a15, a49
	v_pk_add_f32 v[60:61], v[60:61], v[62:63]
	v_pk_mul_f32 v[62:63], v[0:1], v[44:45]
	v_accvgpr_write_b32 a48, v0
	v_accvgpr_read_b32 v89, a45
	v_accvgpr_read_b32 v0, a46
	v_accvgpr_read_b32 v88, a44
	v_accvgpr_read_b32 v1, a47
	v_mov_b32_dpp v39, v68 row_shl:1 row_mask:0xf bank_mask:0xf
	v_pk_fma_f32 v[62:63], v[68:69], v[88:89], v[62:63] op_sel_hi:[0,1,1]
	v_pk_mov_b32 v[68:69], v[68:69], v[0:1] op_sel:[1,0]
	v_mov_b32_e32 v36, v25
	v_pk_fma_f32 v[62:63], v[68:69], v[38:39], v[62:63]
	s_mov_b64 s[0:1], 0x800000
	v_pk_add_f32 v[60:61], v[60:61], v[62:63]
	v_mov_b32_dpp v36, v71 row_shr:1 row_mask:0xf bank_mask:0xf
	v_mov_b32_e32 v65, v71
	v_lshl_add_u64 v[62:63], v[54:55], 0, s[0:1]
	v_mov_b32_e32 v128, v60
	v_mov_b32_e32 v129, v61
	v_pk_mul_f32 v[60:61], v[64:65], v[36:37]
	v_mov_b64_e32 v[118:119], v[86:87]
	v_mov_b32_e32 v12, v7
	v_accvgpr_write_b32 a24, v32
	v_mov_b32_dpp v25, v70 row_shl:1 row_mask:0xf bank_mask:0xf
	v_pk_fma_f32 v[60:61], v[70:71], v[118:119], v[60:61] op_sel_hi:[0,1,1]
	v_mov_b32_e32 v62, v71
	v_mov_b32_e32 v63, v113
	v_mov_b32_dpp v12, v73 row_shr:1 row_mask:0xf bank_mask:0xf
	v_accvgpr_read_b32 v32, a20
	v_mov_b32_e32 v33, v73
	v_pk_fma_f32 v[60:61], v[62:63], v[24:25], v[60:61]
	v_pk_mul_f32 v[62:63], v[32:33], v[12:13]
	v_mov_b32_dpp v7, v72 row_shl:1 row_mask:0xf bank_mask:0xf
	v_pk_fma_f32 v[62:63], v[72:73], v[106:107], v[62:63] op_sel_hi:[0,1,1]
	v_mov_b32_e32 v68, v73
	v_mov_b32_e32 v69, v75
	v_mov_b32_e32 v78, v21
	v_pk_fma_f32 v[62:63], v[68:69], v[6:7], v[62:63]
	v_pk_add_f32 v[60:61], v[60:61], 0 op_sel_hi:[1,0]
	v_mov_b32_dpp v78, v83 row_shr:1 row_mask:0xf bank_mask:0xf
	v_mov_b32_e32 v53, v83
	v_pk_add_f32 v[60:61], v[60:61], v[62:63]
	v_pk_mul_f32 v[62:63], v[52:53], v[78:79]
	v_mov_b32_dpp v21, v82 row_shl:1 row_mask:0xf bank_mask:0xf
	v_pk_fma_f32 v[62:63], v[82:83], v[14:15], v[62:63] op_sel_hi:[0,1,1]
	v_mov_b32_e32 v68, v83
	v_mov_b32_e32 v69, v1
	v_accvgpr_write_b32 a19, v15
	v_pk_fma_f32 v[62:63], v[68:69], v[20:21], v[62:63]
	v_mov_b32_e32 v76, v11
	v_accvgpr_write_b32 a18, v14
	v_pk_add_f32 v[60:61], v[60:61], v[62:63]
	s_mov_b64 s[0:1], 0x810000
	v_mov_b32_dpp v76, v81 row_shr:1 row_mask:0xf bank_mask:0xf
	v_mov_b32_e32 v41, v81
	v_accvgpr_read_b32 v14, a36
	v_accvgpr_write_b32 a6, v2
	v_lshl_add_u64 v[136:137], v[134:135], 0, s[0:1]
	s_nop 1
	s_mov_b64 vcc, s[28:29]
	s_nop 0
	v_cndmask_b32_dpp v130, v60, v128, vcc quad_perm:[1,0,3,2] row_mask:0xf bank_mask:0xf
	v_cndmask_b32_dpp v131, v61, v129, vcc quad_perm:[1,0,3,2] row_mask:0xf bank_mask:0xf
	s_mov_b64 vcc, s[30:31]
	s_nop 0
	v_cndmask_b32_dpp v132, v128, v60, vcc quad_perm:[1,0,3,2] row_mask:0xf bank_mask:0xf
	v_cndmask_b32_dpp v133, v129, v61, vcc quad_perm:[1,0,3,2] row_mask:0xf bank_mask:0xf
	global_store_dwordx4 v[136:137], v[130:133], off sc0 sc1 nt
	s_nop 1
	v_pk_mul_f32 v[60:61], v[40:41], v[76:77]
	v_accvgpr_read_b32 v15, a37
	v_mov_b32_e32 v2, v35
	v_mov_b32_dpp v11, v80 row_shl:1 row_mask:0xf bank_mask:0xf
	v_pk_fma_f32 v[60:61], v[80:81], v[14:15], v[60:61] op_sel_hi:[0,1,1]
	v_pk_mov_b32 v[62:63], v[80:81], v[66:67] op_sel:[1,0]
	v_mov_b32_dpp v2, v85 row_shr:1 row_mask:0xf bank_mask:0xf
	v_mov_b32_e32 v23, v85
	v_accvgpr_read_b32 v15, a9
	v_pk_fma_f32 v[60:61], v[62:63], v[10:11], v[60:61]
	v_pk_mul_f32 v[62:63], v[22:23], v[2:3]
	v_accvgpr_read_b32 v14, a8
	v_mov_b32_dpp v35, v84 row_shl:1 row_mask:0xf bank_mask:0xf
	v_pk_fma_f32 v[62:63], v[84:85], v[100:101], v[62:63] op_sel_hi:[0,1,1]
	v_pk_mov_b32 v[68:69], v[84:85], v[14:15] op_sel:[1,0]
	v_mov_b32_e32 v92, v59
	v_pk_fma_f32 v[62:63], v[68:69], v[34:35], v[62:63]
	v_pk_add_f32 v[60:61], v[60:61], 0 op_sel_hi:[1,0]
	v_mov_b32_dpp v92, v125 row_shr:1 row_mask:0xf bank_mask:0xf
	v_mov_b32_e32 v97, v125
	v_accvgpr_read_b32 v71, a15
	v_pk_add_f32 v[60:61], v[60:61], v[62:63]
	v_pk_mul_f32 v[62:63], v[96:97], v[92:93]
	v_accvgpr_read_b32 v70, a14
	v_mov_b32_dpp v59, v124 row_shl:1 row_mask:0xf bank_mask:0xf
	v_pk_fma_f32 v[62:63], v[124:125], v[16:17], v[62:63] op_sel_hi:[0,1,1]
	v_pk_mov_b32 v[68:69], v[124:125], v[70:71] op_sel:[1,0]
	v_mov_b32_e32 v94, v57
	v_pk_fma_f32 v[62:63], v[68:69], v[58:59], v[62:63]
	s_mov_b64 s[0:1], 0x820000
	v_pk_add_f32 v[60:61], v[60:61], v[62:63]
	v_mov_b32_dpp v94, v123 row_shr:1 row_mask:0xf bank_mask:0xf
	v_mov_b32_e32 v99, v123
	v_accvgpr_write_b32 a31, v17
	v_lshl_add_u64 v[62:63], v[54:55], 0, s[0:1]
	v_mov_b32_e32 v128, v60
	v_mov_b32_e32 v129, v61
	v_pk_mul_f32 v[60:61], v[98:99], v[94:95]
	v_mov_b32_e32 v102, v51
	v_accvgpr_write_b32 a30, v16
	v_mov_b32_dpp v57, v122 row_shl:1 row_mask:0xf bank_mask:0xf
	v_pk_fma_f32 v[60:61], v[122:123], v[28:29], v[60:61] op_sel_hi:[0,1,1]
	v_mov_b32_e32 v62, v123
	v_mov_b32_e32 v63, v67
	v_mov_b32_dpp v102, v121 row_shr:1 row_mask:0xf bank_mask:0xf
	v_mov_b32_e32 v105, v121
	v_accvgpr_read_b32 v16, a28
	v_pk_fma_f32 v[60:61], v[62:63], v[56:57], v[60:61]
	v_pk_mul_f32 v[62:63], v[104:105], v[102:103]
	v_accvgpr_read_b32 v17, a29
	v_mov_b32_dpp v51, v120 row_shl:1 row_mask:0xf bank_mask:0xf
	v_pk_fma_f32 v[62:63], v[120:121], v[16:17], v[62:63] op_sel_hi:[0,1,1]
	v_mov_b32_e32 v68, v121
	v_mov_b32_e32 v69, v15
	v_mov_b32_e32 v108, v49
	v_pk_fma_f32 v[62:63], v[68:69], v[50:51], v[62:63]
	v_pk_add_f32 v[60:61], v[60:61], 0 op_sel_hi:[1,0]
	v_mov_b32_dpp v108, v91 row_shr:1 row_mask:0xf bank_mask:0xf
	v_mov_b32_e32 v111, v91
	v_pk_add_f32 v[60:61], v[60:61], v[62:63]
	v_pk_mul_f32 v[62:63], v[110:111], v[108:109]
	v_mov_b32_dpp v49, v90 row_shl:1 row_mask:0xf bank_mask:0xf
	v_pk_fma_f32 v[62:63], v[90:91], v[30:31], v[62:63] op_sel_hi:[0,1,1]
	v_mov_b32_e32 v68, v91
	v_mov_b32_e32 v69, v71
	v_pk_fma_f32 v[62:63], v[68:69], v[48:49], v[62:63]
	s_mov_b64 s[0:1], 0x830000
	v_mov_b32_e32 v0, v22
	v_pk_add_f32 v[60:61], v[60:61], v[62:63]
	v_lshl_add_u64 v[136:137], v[134:135], 0, s[0:1]
	s_add_u32 s0, s10, 0x1c00000
	v_accvgpr_read_b32 v22, a50
	v_accvgpr_read_b32 v1, a72
	s_addc_u32 s1, s11, 0
	v_accvgpr_read_b32 v23, a51
	s_nop 1
	s_mov_b64 vcc, s[28:29]
	s_nop 0
	v_cndmask_b32_dpp v130, v60, v128, vcc quad_perm:[1,0,3,2] row_mask:0xf bank_mask:0xf
	v_cndmask_b32_dpp v131, v61, v129, vcc quad_perm:[1,0,3,2] row_mask:0xf bank_mask:0xf
	s_mov_b64 vcc, s[30:31]
	s_nop 0
	v_cndmask_b32_dpp v132, v128, v60, vcc quad_perm:[1,0,3,2] row_mask:0xf bank_mask:0xf
	v_cndmask_b32_dpp v133, v129, v61, vcc quad_perm:[1,0,3,2] row_mask:0xf bank_mask:0xf
	global_store_dwordx4 v[136:137], v[130:133], off sc0 sc1 nt
	s_nop 1
	v_readfirstlane_b32 s2, v1
	v_lshl_add_u64 v[60:61], s[0:1], 0, v[22:23]
	v_accvgpr_read_b32 v1, a12
	v_accvgpr_read_b32 v22, a52
	s_waitcnt vmcnt(18)
	s_mov_b32 m0, s2
	v_readfirstlane_b32 s2, v1
	v_accvgpr_read_b32 v23, a53
	v_accvgpr_read_b32 v1, a13
	s_waitcnt lgkmcnt(0)
	s_barrier
	global_load_lds_dwordx4 v[60:61], off nt
	v_lshl_add_u64 v[60:61], s[0:1], 0, v[22:23]
	s_mov_b32 m0, s2
	v_readfirstlane_b32 s2, v1
	v_accvgpr_read_b32 v1, a16
	global_load_lds_dwordx4 v[60:61], off nt
	v_lshl_add_u64 v[60:61], s[0:1], 0, v[114:115]
	s_mov_b32 m0, s2
	v_readfirstlane_b32 s2, v1
	global_load_lds_dwordx4 v[60:61], off nt
	v_lshl_add_u64 v[60:61], s[0:1], 0, v[116:117]
	s_mov_b32 m0, s2
	v_accvgpr_write_b32 a22, v30
	v_accvgpr_write_b32 a44, v70
	global_load_lds_dwordx4 v[60:61], off nt
	v_accvgpr_write_b32 a2, v106
	v_accvgpr_write_b32 a34, v74
	v_accvgpr_write_b32 a23, v31
	v_accvgpr_write_b32 a45, v71
	v_add_u32_e32 v2, 0x7010, v5
	v_mov_b32_e32 v31, v5
	v_add_u32_e32 v5, 0x7000, v4
	ds_read_b64 v[60:61], v2
	ds_read_b64 v[62:63], v2 offset:288
	ds_read_b64 v[68:69], v2 offset:576
	ds_read_b64 v[70:71], v2 offset:1728
	ds_read_b64 v[72:73], v2 offset:2016
	ds_read_b64 v[82:83], v2 offset:2304
	ds_read_b64 v[80:81], v2 offset:3456
	ds_read_b64 v[84:85], v2 offset:3744
	ds_read_b64 v[116:117], v2 offset:4032
	ds_read_b64 v[114:115], v2 offset:5184
	ds_read_b64 v[112:113], v2 offset:5472
	ds_read_b64 v[90:91], v2 offset:5760
	ds_read_b32 v43, v5
	ds_read_b32 v19, v5 offset:288
	ds_read_b32 v39, v5 offset:576
	ds_read_b32 v25, v5 offset:1728
	ds_read_b32 v7, v5 offset:2016
	ds_read_b32 v21, v5 offset:2304
	ds_read_b32 v11, v5 offset:3456
	ds_read_b32 v35, v5 offset:3744
	ds_read_b32 v59, v5 offset:4032
	ds_read_b32 v57, v5 offset:5184
	ds_read_b32 v51, v5 offset:5472
	ds_read_b32 v49, v5 offset:5760
	s_waitcnt lgkmcnt(0)
	v_accvgpr_write_b32 a3, v107
	v_mov_b32_e32 v46, v43
	v_accvgpr_write_b32 a35, v75
	v_accvgpr_read_b32 v74, a40
	v_mov_b32_dpp v46, v61 row_shr:1 row_mask:0xf bank_mask:0xf
	v_mov_b32_e32 v75, v61
	v_accvgpr_read_b32 v107, a39
	v_accvgpr_write_b32 a10, v100
	v_pk_mul_f32 v[86:87], v[74:75], v[46:47]
	v_accvgpr_read_b32 v106, a38
	v_mov_b32_e32 v26, v19
	v_accvgpr_write_b32 a11, v101
	v_mov_b32_dpp v43, v60 row_shl:1 row_mask:0xf bank_mask:0xf
	v_mov_b32_e32 v32, v74
	v_pk_fma_f32 v[86:87], v[60:61], v[8:9], v[86:87] op_sel_hi:[0,1,1]
	v_pk_mov_b32 v[60:61], v[60:61], v[106:107] op_sel:[1,0]
	v_mov_b32_dpp v26, v63 row_shr:1 row_mask:0xf bank_mask:0xf
	v_accvgpr_read_b32 v74, a24
	v_mov_b32_e32 v75, v63
	v_accvgpr_read_b32 v101, a35
	v_pk_fma_f32 v[60:61], v[60:61], v[42:43], v[86:87]
	v_pk_mul_f32 v[86:87], v[74:75], v[26:27]
	v_accvgpr_read_b32 v100, a34
	v_accvgpr_write_b32 a14, v66
	v_mov_b32_dpp v19, v62 row_shl:1 row_mask:0xf bank_mask:0xf
	v_pk_fma_f32 v[86:87], v[62:63], v[126:127], v[86:87] op_sel_hi:[0,1,1]
	v_pk_mov_b32 v[62:63], v[62:63], v[100:101] op_sel:[1,0]
	v_mov_b32_e32 v44, v39
	v_accvgpr_write_b32 a42, v64
	v_accvgpr_write_b32 a15, v67
	v_mov_b32_e32 v66, v4
	v_pk_fma_f32 v[62:63], v[62:63], v[18:19], v[86:87]
	v_pk_add_f32 v[60:61], v[60:61], 0 op_sel_hi:[1,0]
	v_mov_b32_dpp v44, v69 row_shr:1 row_mask:0xf bank_mask:0xf
	v_accvgpr_read_b32 v64, a48
	v_mov_b32_e32 v65, v69
	v_accvgpr_read_b32 v4, a46
	v_pk_add_f32 v[60:61], v[60:61], v[62:63]
	v_pk_mul_f32 v[62:63], v[64:65], v[44:45]
	v_accvgpr_read_b32 v5, a47
	v_mov_b32_dpp v39, v68 row_shl:1 row_mask:0xf bank_mask:0xf
	v_pk_fma_f32 v[62:63], v[68:69], v[88:89], v[62:63] op_sel_hi:[0,1,1]
	v_pk_mov_b32 v[68:69], v[68:69], v[4:5] op_sel:[1,0]
	v_mov_b32_e32 v36, v25
	v_pk_fma_f32 v[62:63], v[68:69], v[38:39], v[62:63]
	s_mov_b64 s[0:1], 0xc00000
	v_pk_add_f32 v[60:61], v[60:61], v[62:63]
	v_mov_b32_dpp v36, v71 row_shr:1 row_mask:0xf bank_mask:0xf
	v_accvgpr_read_b32 v22, a42
	v_mov_b32_e32 v23, v71
	v_accvgpr_mov_b32 a26, a20
	v_accvgpr_write_b32 a20, v28
	v_lshl_add_u64 v[62:63], v[54:55], 0, s[0:1]
	v_mov_b32_e32 v128, v60
	v_mov_b32_e32 v129, v61
	v_pk_mul_f32 v[60:61], v[22:23], v[36:37]
	v_mov_b32_e32 v12, v7
	v_accvgpr_write_b32 a21, v29
	v_mov_b32_dpp v25, v70 row_shl:1 row_mask:0xf bank_mask:0xf
	v_pk_fma_f32 v[60:61], v[70:71], v[118:119], v[60:61] op_sel_hi:[0,1,1]
	v_mov_b32_e32 v62, v71
	v_mov_b32_e32 v63, v107
	v_mov_b32_dpp v12, v73 row_shr:1 row_mask:0xf bank_mask:0xf
	v_accvgpr_read_b32 v28, a26
	v_mov_b32_e32 v29, v73
	v_accvgpr_read_b32 v121, a3
	v_pk_fma_f32 v[60:61], v[62:63], v[24:25], v[60:61]
	v_pk_mul_f32 v[62:63], v[28:29], v[12:13]
	v_accvgpr_read_b32 v120, a2
	v_mov_b32_dpp v7, v72 row_shl:1 row_mask:0xf bank_mask:0xf
	v_pk_fma_f32 v[62:63], v[72:73], v[120:121], v[62:63] op_sel_hi:[0,1,1]
	v_mov_b32_e32 v68, v73
	v_mov_b32_e32 v69, v101
	v_mov_b32_e32 v78, v21
	v_pk_fma_f32 v[62:63], v[68:69], v[6:7], v[62:63]
	v_pk_add_f32 v[60:61], v[60:61], 0 op_sel_hi:[1,0]
	v_mov_b32_dpp v78, v83 row_shr:1 row_mask:0xf bank_mask:0xf
	v_mov_b32_e32 v53, v83
	v_accvgpr_read_b32 v125, a19
	v_pk_add_f32 v[60:61], v[60:61], v[62:63]
	v_pk_mul_f32 v[62:63], v[52:53], v[78:79]
	v_accvgpr_read_b32 v124, a18
	v_mov_b32_dpp v21, v82 row_shl:1 row_mask:0xf bank_mask:0xf
	v_pk_fma_f32 v[62:63], v[82:83], v[124:125], v[62:63] op_sel_hi:[0,1,1]
	v_mov_b32_e32 v68, v83
	v_mov_b32_e32 v69, v5
	v_pk_fma_f32 v[62:63], v[68:69], v[20:21], v[62:63]
	v_mov_b32_e32 v76, v11
	v_pk_add_f32 v[60:61], v[60:61], v[62:63]
	s_mov_b64 s[0:1], 0xc10000
	v_mov_b32_dpp v76, v81 row_shr:1 row_mask:0xf bank_mask:0xf
	v_mov_b32_e32 v41, v81
	v_accvgpr_read_b32 v123, a37
	v_accvgpr_read_b32 v4, a14
	v_lshl_add_u64 v[136:137], v[134:135], 0, s[0:1]
	s_nop 1
	s_mov_b64 vcc, s[28:29]
	s_nop 0
	v_cndmask_b32_dpp v130, v60, v128, vcc quad_perm:[1,0,3,2] row_mask:0xf bank_mask:0xf
	v_cndmask_b32_dpp v131, v61, v129, vcc quad_perm:[1,0,3,2] row_mask:0xf bank_mask:0xf
	s_mov_b64 vcc, s[30:31]
	s_nop 0
	v_cndmask_b32_dpp v132, v128, v60, vcc quad_perm:[1,0,3,2] row_mask:0xf bank_mask:0xf
	v_cndmask_b32_dpp v133, v129, v61, vcc quad_perm:[1,0,3,2] row_mask:0xf bank_mask:0xf
	global_store_dwordx4 v[136:137], v[130:133], off sc0 sc1 nt
	s_nop 1
	v_pk_mul_f32 v[60:61], v[40:41], v[76:77]
	v_accvgpr_read_b32 v122, a36
	v_accvgpr_read_b32 v5, a15
	v_mov_b32_e32 v2, v35
	v_accvgpr_mov_b32 a32, a24
	v_accvgpr_write_b32 a24, v22
	v_mov_b64_e32 v[22:23], v[118:119]
	v_mov_b32_dpp v11, v80 row_shl:1 row_mask:0xf bank_mask:0xf
	v_pk_fma_f32 v[60:61], v[80:81], v[122:123], v[60:61] op_sel_hi:[0,1,1]
	v_pk_mov_b32 v[62:63], v[80:81], v[4:5] op_sel:[1,0]
	v_mov_b32_dpp v2, v85 row_shr:1 row_mask:0xf bank_mask:0xf
	v_mov_b32_e32 v106, v0
	v_mov_b32_e32 v107, v85
	v_accvgpr_read_b32 v119, a11
	v_pk_fma_f32 v[60:61], v[62:63], v[10:11], v[60:61]
	v_pk_mul_f32 v[62:63], v[106:107], v[2:3]
	v_accvgpr_read_b32 v118, a10
	v_mov_b64_e32 v[100:101], v[14:15]
	v_mov_b32_dpp v35, v84 row_shl:1 row_mask:0xf bank_mask:0xf
	v_pk_fma_f32 v[62:63], v[84:85], v[118:119], v[62:63] op_sel_hi:[0,1,1]
	v_pk_mov_b32 v[68:69], v[84:85], v[100:101] op_sel:[1,0]
	v_mov_b32_e32 v92, v59
	v_accvgpr_write_b32 a26, v52
	v_mov_b32_e32 v74, v40
	v_pk_fma_f32 v[62:63], v[68:69], v[34:35], v[62:63]
	v_pk_add_f32 v[60:61], v[60:61], 0 op_sel_hi:[1,0]
	v_mov_b32_dpp v92, v117 row_shr:1 row_mask:0xf bank_mask:0xf
	v_mov_b32_e32 v97, v117
	v_accvgpr_read_b32 v41, a31
	v_accvgpr_read_b32 v53, a45
	v_pk_add_f32 v[60:61], v[60:61], v[62:63]
	v_pk_mul_f32 v[62:63], v[96:97], v[92:93]
	v_accvgpr_read_b32 v40, a30
	v_accvgpr_read_b32 v52, a44
	v_mov_b32_dpp v59, v116 row_shl:1 row_mask:0xf bank_mask:0xf
	v_pk_fma_f32 v[62:63], v[116:117], v[40:41], v[62:63] op_sel_hi:[0,1,1]
	v_pk_mov_b32 v[68:69], v[116:117], v[52:53] op_sel:[1,0]
	v_mov_b32_e32 v94, v57
	v_pk_fma_f32 v[62:63], v[68:69], v[58:59], v[62:63]
	s_mov_b64 s[0:1], 0xc20000
	v_pk_add_f32 v[60:61], v[60:61], v[62:63]
	v_mov_b32_dpp v94, v115 row_shr:1 row_mask:0xf bank_mask:0xf
	v_mov_b32_e32 v99, v115
	v_accvgpr_read_b32 v14, a20
	v_lshl_add_u64 v[62:63], v[54:55], 0, s[0:1]
	v_mov_b32_e32 v128, v60
	v_mov_b32_e32 v129, v61
	v_pk_mul_f32 v[60:61], v[98:99], v[94:95]
	v_accvgpr_read_b32 v15, a21
	v_mov_b32_e32 v102, v51
	v_mov_b32_dpp v57, v114 row_shl:1 row_mask:0xf bank_mask:0xf
	v_pk_fma_f32 v[60:61], v[114:115], v[14:15], v[60:61] op_sel_hi:[0,1,1]
	v_mov_b32_e32 v62, v115
	v_mov_b32_e32 v63, v5
	v_mov_b32_dpp v102, v113 row_shr:1 row_mask:0xf bank_mask:0xf
	v_mov_b32_e32 v105, v113
	v_pk_fma_f32 v[60:61], v[62:63], v[56:57], v[60:61]
	v_pk_mul_f32 v[62:63], v[104:105], v[102:103]
	v_accvgpr_write_b32 a8, v8
	v_mov_b32_dpp v51, v112 row_shl:1 row_mask:0xf bank_mask:0xf
	v_pk_fma_f32 v[62:63], v[112:113], v[16:17], v[62:63] op_sel_hi:[0,1,1]
	v_mov_b32_e32 v68, v113
	v_mov_b32_e32 v69, v101
	v_mov_b32_e32 v108, v49
	v_accvgpr_write_b32 a9, v9
	v_pk_fma_f32 v[62:63], v[68:69], v[50:51], v[62:63]
	v_pk_add_f32 v[60:61], v[60:61], 0 op_sel_hi:[1,0]
	v_mov_b32_dpp v108, v91 row_shr:1 row_mask:0xf bank_mask:0xf
	v_mov_b32_e32 v111, v91
	v_accvgpr_read_b32 v8, a22
	v_pk_add_f32 v[60:61], v[60:61], v[62:63]
	v_pk_mul_f32 v[62:63], v[110:111], v[108:109]
	v_accvgpr_read_b32 v9, a23
	v_mov_b32_dpp v49, v90 row_shl:1 row_mask:0xf bank_mask:0xf
	v_pk_fma_f32 v[62:63], v[90:91], v[8:9], v[62:63] op_sel_hi:[0,1,1]
	v_mov_b32_e32 v68, v91
	v_mov_b32_e32 v69, v53
	v_pk_fma_f32 v[62:63], v[68:69], v[48:49], v[62:63]
	s_mov_b64 s[0:1], 0xc30000
	v_pk_add_f32 v[60:61], v[60:61], v[62:63]
	v_lshl_add_u64 v[136:137], v[134:135], 0, s[0:1]
	s_nop 1
	s_mov_b64 vcc, s[28:29]
	s_nop 0
	v_cndmask_b32_dpp v130, v60, v128, vcc quad_perm:[1,0,3,2] row_mask:0xf bank_mask:0xf
	v_cndmask_b32_dpp v131, v61, v129, vcc quad_perm:[1,0,3,2] row_mask:0xf bank_mask:0xf
	s_mov_b64 vcc, s[30:31]
	s_nop 0
	v_cndmask_b32_dpp v132, v128, v60, vcc quad_perm:[1,0,3,2] row_mask:0xf bank_mask:0xf
	v_cndmask_b32_dpp v133, v129, v61, vcc quad_perm:[1,0,3,2] row_mask:0xf bank_mask:0xf
	global_store_dwordx4 v[136:137], v[130:133], off sc0 sc1 nt
	s_nop 1
	s_waitcnt vmcnt(20)
	v_accvgpr_write_b32 a16, v88
	v_accvgpr_write_b32 a10, v100
	s_waitcnt lgkmcnt(0)
	s_barrier
	v_add_u32_e32 v2, 0xe010, v31
	v_add_u32_e32 v5, 0xe000, v66
	ds_read_b64 v[60:61], v2
	ds_read_b64 v[62:63], v2 offset:288
	ds_read_b64 v[68:69], v2 offset:576
	ds_read_b64 v[70:71], v2 offset:1728
	ds_read_b64 v[72:73], v2 offset:2016
	ds_read_b64 v[82:83], v2 offset:2304
	ds_read_b64 v[80:81], v2 offset:3456
	ds_read_b64 v[84:85], v2 offset:3744
	ds_read_b64 v[116:117], v2 offset:4032
	ds_read_b64 v[114:115], v2 offset:5184
	ds_read_b64 v[112:113], v2 offset:5472
	ds_read_b64 v[90:91], v2 offset:5760
	ds_read_b32 v43, v5
	ds_read_b32 v19, v5 offset:288
	ds_read_b32 v39, v5 offset:576
	ds_read_b32 v25, v5 offset:1728
	ds_read_b32 v7, v5 offset:2016
	ds_read_b32 v21, v5 offset:2304
	ds_read_b32 v11, v5 offset:3456
	ds_read_b32 v35, v5 offset:3744
	ds_read_b32 v59, v5 offset:4032
	ds_read_b32 v57, v5 offset:5184
	ds_read_b32 v51, v5 offset:5472
	ds_read_b32 v49, v5 offset:5760
	s_waitcnt lgkmcnt(0)
	v_accvgpr_write_b32 a17, v89
	v_mov_b32_e32 v46, v43
	v_accvgpr_write_b32 a11, v101
	v_mov_b32_e32 v33, v61
	v_mov_b32_dpp v46, v61 row_shr:1 row_mask:0xf bank_mask:0xf
	v_accvgpr_read_b32 v89, a9
	v_accvgpr_read_b32 v101, a39
	v_pk_mul_f32 v[86:87], v[32:33], v[46:47]
	v_accvgpr_read_b32 v88, a8
	v_accvgpr_read_b32 v100, a38
	v_mov_b32_e32 v26, v19
	v_accvgpr_write_b32 a19, v17
	v_mov_b32_dpp v43, v60 row_shl:1 row_mask:0xf bank_mask:0xf
	v_pk_fma_f32 v[86:87], v[60:61], v[88:89], v[86:87] op_sel_hi:[0,1,1]
	v_pk_mov_b32 v[60:61], v[60:61], v[100:101] op_sel:[1,0]
	v_mov_b32_dpp v26, v63 row_shr:1 row_mask:0xf bank_mask:0xf
	v_accvgpr_read_b32 v0, a32
	v_mov_b32_e32 v1, v63
	v_accvgpr_read_b32 v4, a34
	v_accvgpr_write_b32 a18, v16
	v_pk_fma_f32 v[60:61], v[60:61], v[42:43], v[86:87]
	v_pk_mul_f32 v[86:87], v[0:1], v[26:27]
	v_mov_b64_e32 v[16:17], v[126:127]
	v_accvgpr_read_b32 v5, a35
	v_mov_b32_dpp v19, v62 row_shl:1 row_mask:0xf bank_mask:0xf
	v_pk_fma_f32 v[86:87], v[62:63], v[16:17], v[86:87] op_sel_hi:[0,1,1]
	v_pk_mov_b32 v[62:63], v[62:63], v[4:5] op_sel:[1,0]
	v_mov_b32_e32 v44, v39
	v_accvgpr_read_b32 v30, a48
	v_mov_b32_e32 v64, v28
	v_accvgpr_write_b32 a7, v66
	v_pk_fma_f32 v[62:63], v[62:63], v[18:19], v[86:87]
	v_pk_add_f32 v[60:61], v[60:61], 0 op_sel_hi:[1,0]
	v_mov_b32_dpp v44, v69 row_shr:1 row_mask:0xf bank_mask:0xf
	v_mov_b32_e32 v31, v69
	v_accvgpr_read_b32 v29, a17
	v_accvgpr_read_b32 v67, a47
	v_pk_add_f32 v[60:61], v[60:61], v[62:63]
	v_pk_mul_f32 v[62:63], v[30:31], v[44:45]
	v_accvgpr_read_b32 v28, a16
	v_accvgpr_read_b32 v66, a46
	v_mov_b32_dpp v39, v68 row_shl:1 row_mask:0xf bank_mask:0xf
	v_pk_fma_f32 v[62:63], v[68:69], v[28:29], v[62:63] op_sel_hi:[0,1,1]
	v_pk_mov_b32 v[68:69], v[68:69], v[66:67] op_sel:[1,0]
	v_mov_b32_e32 v36, v25
	v_pk_fma_f32 v[62:63], v[68:69], v[38:39], v[62:63]
	s_mov_b64 s[0:1], 0x1000000
	v_pk_add_f32 v[60:61], v[60:61], v[62:63]
	v_mov_b32_dpp v36, v71 row_shr:1 row_mask:0xf bank_mask:0xf
	v_accvgpr_read_b32 v126, a24
	v_mov_b32_e32 v127, v71
	v_lshl_add_u64 v[62:63], v[54:55], 0, s[0:1]
	v_mov_b32_e32 v128, v60
	v_mov_b32_e32 v129, v61
	v_pk_mul_f32 v[60:61], v[126:127], v[36:37]
	v_mov_b32_e32 v12, v7
	v_mov_b32_dpp v25, v70 row_shl:1 row_mask:0xf bank_mask:0xf
	v_pk_fma_f32 v[60:61], v[70:71], v[22:23], v[60:61] op_sel_hi:[0,1,1]
	v_mov_b32_e32 v62, v71
	v_mov_b32_e32 v63, v101
	v_mov_b32_dpp v12, v73 row_shr:1 row_mask:0xf bank_mask:0xf
	v_mov_b32_e32 v52, v64
	v_mov_b32_e32 v53, v73
	v_pk_fma_f32 v[60:61], v[62:63], v[24:25], v[60:61]
	v_pk_mul_f32 v[62:63], v[52:53], v[12:13]
	v_mov_b32_dpp v7, v72 row_shl:1 row_mask:0xf bank_mask:0xf
	v_pk_fma_f32 v[62:63], v[72:73], v[120:121], v[62:63] op_sel_hi:[0,1,1]
	v_mov_b32_e32 v68, v73
	v_mov_b32_e32 v69, v5
	v_mov_b32_e32 v78, v21
	v_pk_fma_f32 v[62:63], v[68:69], v[6:7], v[62:63]
	v_pk_add_f32 v[60:61], v[60:61], 0 op_sel_hi:[1,0]
	v_mov_b32_dpp v78, v83 row_shr:1 row_mask:0xf bank_mask:0xf
	v_accvgpr_read_b32 v4, a26
	v_mov_b32_e32 v5, v83
	v_pk_add_f32 v[60:61], v[60:61], v[62:63]
	v_pk_mul_f32 v[62:63], v[4:5], v[78:79]
	v_mov_b32_dpp v21, v82 row_shl:1 row_mask:0xf bank_mask:0xf
	v_pk_fma_f32 v[62:63], v[82:83], v[124:125], v[62:63] op_sel_hi:[0,1,1]
	v_mov_b32_e32 v68, v83
	v_mov_b32_e32 v69, v67
	v_accvgpr_write_b32 a8, v120
	v_pk_fma_f32 v[62:63], v[68:69], v[20:21], v[62:63]
	v_mov_b32_e32 v76, v11
	v_accvgpr_write_b32 a9, v121
	v_pk_add_f32 v[60:61], v[60:61], v[62:63]
	s_mov_b64 s[0:1], 0x1010000
	v_mov_b32_dpp v76, v81 row_shr:1 row_mask:0xf bank_mask:0xf
	v_mov_b32_e32 v120, v74
	v_mov_b32_e32 v121, v81
	v_accvgpr_read_b32 v101, a15
	v_accvgpr_mov_b32 a12, a38
	v_lshl_add_u64 v[136:137], v[134:135], 0, s[0:1]
	s_nop 1
	s_mov_b64 vcc, s[28:29]
	s_nop 0
	v_cndmask_b32_dpp v130, v60, v128, vcc quad_perm:[1,0,3,2] row_mask:0xf bank_mask:0xf
	v_cndmask_b32_dpp v131, v61, v129, vcc quad_perm:[1,0,3,2] row_mask:0xf bank_mask:0xf
	s_mov_b64 vcc, s[30:31]
	s_nop 0
	v_cndmask_b32_dpp v132, v128, v60, vcc quad_perm:[1,0,3,2] row_mask:0xf bank_mask:0xf
	v_cndmask_b32_dpp v133, v129, v61, vcc quad_perm:[1,0,3,2] row_mask:0xf bank_mask:0xf
	global_store_dwordx4 v[136:137], v[130:133], off sc0 sc1 nt
	s_nop 1
	v_pk_mul_f32 v[60:61], v[120:121], v[76:77]
	v_accvgpr_read_b32 v100, a14
	v_mov_b32_e32 v2, v35
	v_accvgpr_mov_b32 a13, a39
	v_accvgpr_write_b32 a20, v22
	v_mov_b32_dpp v11, v80 row_shl:1 row_mask:0xf bank_mask:0xf
	v_pk_fma_f32 v[60:61], v[80:81], v[122:123], v[60:61] op_sel_hi:[0,1,1]
	v_pk_mov_b32 v[62:63], v[80:81], v[100:101] op_sel:[1,0]
	v_mov_b32_dpp v2, v85 row_shr:1 row_mask:0xf bank_mask:0xf
	v_mov_b32_e32 v107, v85
	v_accvgpr_read_b32 v123, a11
	v_accvgpr_write_b32 a21, v23
	v_accvgpr_read_b32 v23, a13
	v_pk_fma_f32 v[60:61], v[62:63], v[10:11], v[60:61]
	v_pk_mul_f32 v[62:63], v[106:107], v[2:3]
	v_accvgpr_read_b32 v122, a10
	v_accvgpr_read_b32 v22, a12
	v_mov_b32_dpp v35, v84 row_shl:1 row_mask:0xf bank_mask:0xf
	v_pk_fma_f32 v[62:63], v[84:85], v[118:119], v[62:63] op_sel_hi:[0,1,1]
	v_accvgpr_write_b32 a12, v118
	v_pk_mov_b32 v[68:69], v[84:85], v[122:123] op_sel:[1,0]
	v_mov_b32_e32 v92, v59
	v_accvgpr_write_b32 a13, v119
	v_pk_fma_f32 v[62:63], v[68:69], v[34:35], v[62:63]
	v_pk_add_f32 v[60:61], v[60:61], 0 op_sel_hi:[1,0]
	v_mov_b32_dpp v92, v117 row_shr:1 row_mask:0xf bank_mask:0xf
	v_mov_b32_e32 v97, v117
	v_mov_b64_e32 v[118:119], v[40:41]
	v_accvgpr_read_b32 v40, a44
	v_pk_add_f32 v[60:61], v[60:61], v[62:63]
	v_pk_mul_f32 v[62:63], v[96:97], v[92:93]
	v_accvgpr_read_b32 v41, a45
	v_mov_b32_dpp v59, v116 row_shl:1 row_mask:0xf bank_mask:0xf
	v_pk_fma_f32 v[62:63], v[116:117], v[118:119], v[62:63] op_sel_hi:[0,1,1]
	v_pk_mov_b32 v[68:69], v[116:117], v[40:41] op_sel:[1,0]
	v_mov_b32_e32 v94, v57
	v_pk_fma_f32 v[62:63], v[68:69], v[58:59], v[62:63]
	s_mov_b64 s[0:1], 0x1020000
	v_pk_add_f32 v[60:61], v[60:61], v[62:63]
	v_mov_b32_dpp v94, v115 row_shr:1 row_mask:0xf bank_mask:0xf
	v_mov_b32_e32 v99, v115
	v_lshl_add_u64 v[62:63], v[54:55], 0, s[0:1]
	v_mov_b32_e32 v128, v60
	v_mov_b32_e32 v129, v61
	v_pk_mul_f32 v[60:61], v[98:99], v[94:95]
	v_mov_b32_e32 v102, v51
	v_accvgpr_write_b32 a30, v4
	v_mov_b32_dpp v57, v114 row_shl:1 row_mask:0xf bank_mask:0xf
	v_pk_fma_f32 v[60:61], v[114:115], v[14:15], v[60:61] op_sel_hi:[0,1,1]
	v_mov_b32_e32 v62, v115
	v_mov_b32_e32 v63, v101
	v_mov_b32_dpp v102, v113 row_shr:1 row_mask:0xf bank_mask:0xf
	v_mov_b32_e32 v105, v113
	v_accvgpr_read_b32 v4, a18
	v_pk_fma_f32 v[60:61], v[62:63], v[56:57], v[60:61]
	v_pk_mul_f32 v[62:63], v[104:105], v[102:103]
	v_accvgpr_read_b32 v5, a19
	v_mov_b32_dpp v51, v112 row_shl:1 row_mask:0xf bank_mask:0xf
	v_pk_fma_f32 v[62:63], v[112:113], v[4:5], v[62:63] op_sel_hi:[0,1,1]
	v_mov_b32_e32 v68, v113
	v_mov_b32_e32 v69, v123
	v_mov_b32_e32 v108, v49
	v_pk_fma_f32 v[62:63], v[68:69], v[50:51], v[62:63]
	v_pk_add_f32 v[60:61], v[60:61], 0 op_sel_hi:[1,0]
	v_mov_b32_dpp v108, v91 row_shr:1 row_mask:0xf bank_mask:0xf
	v_mov_b32_e32 v111, v91
	v_pk_add_f32 v[60:61], v[60:61], v[62:63]
	v_pk_mul_f32 v[62:63], v[110:111], v[108:109]
	v_mov_b32_dpp v49, v90 row_shl:1 row_mask:0xf bank_mask:0xf
	v_pk_fma_f32 v[62:63], v[90:91], v[8:9], v[62:63] op_sel_hi:[0,1,1]
	v_mov_b32_e32 v68, v91
	v_mov_b32_e32 v69, v41
	v_pk_fma_f32 v[62:63], v[68:69], v[48:49], v[62:63]
	s_mov_b64 s[0:1], 0x1030000
	v_pk_add_f32 v[60:61], v[60:61], v[62:63]
	v_lshl_add_u64 v[136:137], v[134:135], 0, s[0:1]
	s_nop 1
	s_mov_b64 vcc, s[28:29]
	s_nop 0
	v_cndmask_b32_dpp v130, v60, v128, vcc quad_perm:[1,0,3,2] row_mask:0xf bank_mask:0xf
	v_cndmask_b32_dpp v131, v61, v129, vcc quad_perm:[1,0,3,2] row_mask:0xf bank_mask:0xf
	s_mov_b64 vcc, s[30:31]
	s_nop 0
	v_cndmask_b32_dpp v132, v128, v60, vcc quad_perm:[1,0,3,2] row_mask:0xf bank_mask:0xf
	v_cndmask_b32_dpp v133, v129, v61, vcc quad_perm:[1,0,3,2] row_mask:0xf bank_mask:0xf
	global_store_dwordx4 v[136:137], v[130:133], off sc0 sc1 nt
	s_nop 1
	s_waitcnt vmcnt(16)
	s_waitcnt lgkmcnt(0)
	s_barrier
	v_accvgpr_read_b32 v2, a0
	v_accvgpr_read_b32 v8, a4
	ds_read_b64 v[60:61], v8
	ds_read_b64 v[62:63], v8 offset:288
	ds_read_b64 v[68:69], v8 offset:576
	ds_read_b64 v[70:71], v8 offset:1728
	ds_read_b64 v[72:73], v8 offset:2016
	ds_read_b64 v[82:83], v8 offset:2304
	ds_read_b64 v[80:81], v8 offset:3456
	ds_read_b64 v[84:85], v8 offset:3744
	ds_read_b64 v[116:117], v8 offset:4032
	ds_read_b64 v[114:115], v8 offset:5184
	ds_read_b64 v[112:113], v8 offset:5472
	ds_read_b64 v[90:91], v8 offset:5760
	ds_read_b32 v43, v2
	ds_read_b32 v19, v2 offset:288
	ds_read_b32 v39, v2 offset:576
	ds_read_b32 v25, v2 offset:1728
	ds_read_b32 v7, v2 offset:2016
	ds_read_b32 v21, v2 offset:2304
	ds_read_b32 v11, v2 offset:3456
	ds_read_b32 v35, v2 offset:3744
	ds_read_b32 v59, v2 offset:4032
	ds_read_b32 v57, v2 offset:5184
	ds_read_b32 v51, v2 offset:5472
	ds_read_b32 v49, v2 offset:5760
	s_waitcnt lgkmcnt(0)
	v_mov_b32_e32 v64, v32
	v_mov_b32_e32 v46, v43
	v_mov_b32_e32 v65, v61
	v_mov_b64_e32 v[100:101], v[22:23]
	v_mov_b32_dpp v46, v61 row_shr:1 row_mask:0xf bank_mask:0xf
	v_pk_mul_f32 v[86:87], v[64:65], v[46:47]
	v_mov_b32_e32 v26, v19
	v_mov_b32_dpp v43, v60 row_shl:1 row_mask:0xf bank_mask:0xf
	v_pk_fma_f32 v[86:87], v[60:61], v[88:89], v[86:87] op_sel_hi:[0,1,1]
	v_pk_mov_b32 v[60:61], v[60:61], v[100:101] op_sel:[1,0]
	v_mov_b32_dpp v26, v63 row_shr:1 row_mask:0xf bank_mask:0xf
	v_mov_b32_e32 v1, v63
	v_accvgpr_read_b32 v67, a35
	v_pk_fma_f32 v[60:61], v[60:61], v[42:43], v[86:87]
	v_pk_mul_f32 v[86:87], v[0:1], v[26:27]
	v_accvgpr_read_b32 v66, a34
	v_accvgpr_write_b32 a10, v14
	v_mov_b32_dpp v19, v62 row_shl:1 row_mask:0xf bank_mask:0xf
	v_pk_fma_f32 v[86:87], v[62:63], v[16:17], v[86:87] op_sel_hi:[0,1,1]
	v_pk_mov_b32 v[62:63], v[62:63], v[66:67] op_sel:[1,0]
	v_mov_b32_e32 v44, v39
	v_accvgpr_write_b32 a11, v15
	v_pk_fma_f32 v[62:63], v[62:63], v[18:19], v[86:87]
	v_pk_add_f32 v[60:61], v[60:61], 0 op_sel_hi:[1,0]
	v_mov_b32_dpp v44, v69 row_shr:1 row_mask:0xf bank_mask:0xf
	v_mov_b32_e32 v31, v69
	v_accvgpr_read_b32 v14, a16
	v_accvgpr_read_b32 v28, a46
	v_pk_add_f32 v[60:61], v[60:61], v[62:63]
	v_pk_mul_f32 v[62:63], v[30:31], v[44:45]
	v_accvgpr_read_b32 v15, a17
	v_accvgpr_read_b32 v29, a47
	v_mov_b32_dpp v39, v68 row_shl:1 row_mask:0xf bank_mask:0xf
	v_pk_fma_f32 v[62:63], v[68:69], v[14:15], v[62:63] op_sel_hi:[0,1,1]
	v_pk_mov_b32 v[68:69], v[68:69], v[28:29] op_sel:[1,0]
	v_mov_b32_e32 v36, v25
	v_pk_fma_f32 v[62:63], v[68:69], v[38:39], v[62:63]
	s_mov_b64 s[0:1], 0x1400000
	v_pk_add_f32 v[60:61], v[60:61], v[62:63]
	v_mov_b32_dpp v36, v71 row_shr:1 row_mask:0xf bank_mask:0xf
	v_mov_b32_e32 v127, v71
	v_accvgpr_read_b32 v8, a20
	v_lshl_add_u64 v[62:63], v[54:55], 0, s[0:1]
	v_mov_b32_e32 v128, v60
	v_mov_b32_e32 v129, v61
	v_pk_mul_f32 v[60:61], v[126:127], v[36:37]
	v_accvgpr_read_b32 v9, a21
	v_accvgpr_write_b32 a25, v23
	v_mov_b32_e32 v12, v7
	v_mov_b32_dpp v25, v70 row_shl:1 row_mask:0xf bank_mask:0xf
	v_pk_fma_f32 v[60:61], v[70:71], v[8:9], v[60:61] op_sel_hi:[0,1,1]
	v_mov_b32_e32 v62, v71
	v_mov_b32_e32 v63, v101
	v_accvgpr_write_b32 a24, v22
	v_mov_b32_dpp v12, v73 row_shr:1 row_mask:0xf bank_mask:0xf
	v_mov_b32_e32 v74, v52
	v_mov_b32_e32 v75, v73
	v_accvgpr_read_b32 v23, a9
	v_accvgpr_write_b32 a26, v124
	v_accvgpr_mov_b32 a2, a22
	v_pk_fma_f32 v[60:61], v[62:63], v[24:25], v[60:61]
	v_pk_mul_f32 v[62:63], v[74:75], v[12:13]
	v_accvgpr_read_b32 v22, a8
	v_accvgpr_write_b32 a27, v125
	v_accvgpr_mov_b32 a3, a23
	v_accvgpr_write_b32 a22, v88
	v_mov_b32_dpp v7, v72 row_shl:1 row_mask:0xf bank_mask:0xf
	v_pk_fma_f32 v[62:63], v[72:73], v[22:23], v[62:63] op_sel_hi:[0,1,1]
	v_mov_b32_e32 v68, v73
	v_mov_b32_e32 v69, v67
	v_mov_b32_e32 v78, v21
	v_accvgpr_write_b32 a23, v89
	v_pk_fma_f32 v[62:63], v[68:69], v[6:7], v[62:63]
	v_pk_add_f32 v[60:61], v[60:61], 0 op_sel_hi:[1,0]
	v_mov_b32_dpp v78, v83 row_shr:1 row_mask:0xf bank_mask:0xf
	v_accvgpr_read_b32 v52, a30
	v_mov_b32_e32 v53, v83
	v_accvgpr_read_b32 v89, a27
	v_pk_add_f32 v[60:61], v[60:61], v[62:63]
	v_pk_mul_f32 v[62:63], v[52:53], v[78:79]
	v_accvgpr_read_b32 v88, a26
	v_mov_b32_dpp v21, v82 row_shl:1 row_mask:0xf bank_mask:0xf
	v_pk_fma_f32 v[62:63], v[82:83], v[88:89], v[62:63] op_sel_hi:[0,1,1]
	v_mov_b32_e32 v68, v83
	v_mov_b32_e32 v69, v29
	v_pk_fma_f32 v[62:63], v[68:69], v[20:21], v[62:63]
	v_mov_b32_e32 v76, v11
	v_accvgpr_read_b32 v125, a37
	v_pk_add_f32 v[60:61], v[60:61], v[62:63]
	s_mov_b64 s[0:1], 0x1410000
	v_mov_b32_dpp v76, v81 row_shr:1 row_mask:0xf bank_mask:0xf
	v_mov_b32_e32 v121, v81
	v_accvgpr_read_b32 v101, a15
	v_accvgpr_read_b32 v124, a36
	v_lshl_add_u64 v[136:137], v[134:135], 0, s[0:1]
	s_nop 1
	s_mov_b64 vcc, s[28:29]
	s_nop 0
	v_cndmask_b32_dpp v130, v60, v128, vcc quad_perm:[1,0,3,2] row_mask:0xf bank_mask:0xf
	v_cndmask_b32_dpp v131, v61, v129, vcc quad_perm:[1,0,3,2] row_mask:0xf bank_mask:0xf
	s_mov_b64 vcc, s[30:31]
	s_nop 0
	v_cndmask_b32_dpp v132, v128, v60, vcc quad_perm:[1,0,3,2] row_mask:0xf bank_mask:0xf
	v_cndmask_b32_dpp v133, v129, v61, vcc quad_perm:[1,0,3,2] row_mask:0xf bank_mask:0xf
	global_store_dwordx4 v[136:137], v[130:133], off sc0 sc1 nt
	s_nop 1
	v_pk_mul_f32 v[60:61], v[120:121], v[76:77]
	v_accvgpr_read_b32 v100, a14
	v_mov_b32_e32 v2, v35
	v_mov_b32_dpp v11, v80 row_shl:1 row_mask:0xf bank_mask:0xf
	v_pk_fma_f32 v[60:61], v[80:81], v[124:125], v[60:61] op_sel_hi:[0,1,1]
	v_pk_mov_b32 v[62:63], v[80:81], v[100:101] op_sel:[1,0]
	v_mov_b32_dpp v2, v85 row_shr:1 row_mask:0xf bank_mask:0xf
	v_mov_b32_e32 v107, v85
	v_accvgpr_read_b32 v29, a13
	v_pk_fma_f32 v[60:61], v[62:63], v[10:11], v[60:61]
	v_pk_mul_f32 v[62:63], v[106:107], v[2:3]
	v_accvgpr_read_b32 v28, a12
	v_mov_b32_dpp v35, v84 row_shl:1 row_mask:0xf bank_mask:0xf
	v_pk_fma_f32 v[62:63], v[84:85], v[28:29], v[62:63] op_sel_hi:[0,1,1]
	v_pk_mov_b32 v[68:69], v[84:85], v[122:123] op_sel:[1,0]
	v_mov_b32_e32 v92, v59
	v_pk_fma_f32 v[62:63], v[68:69], v[34:35], v[62:63]
	v_pk_add_f32 v[60:61], v[60:61], 0 op_sel_hi:[1,0]
	v_mov_b32_dpp v92, v117 row_shr:1 row_mask:0xf bank_mask:0xf
	v_mov_b32_e32 v97, v117
	v_pk_add_f32 v[60:61], v[60:61], v[62:63]
	v_pk_mul_f32 v[62:63], v[96:97], v[92:93]
	v_accvgpr_write_b32 a8, v118
	v_pk_fma_f32 v[62:63], v[116:117], v[118:119], v[62:63] op_sel_hi:[0,1,1]
	v_accvgpr_write_b32 a9, v119
	v_accvgpr_read_b32 v119, a45
	v_accvgpr_read_b32 v118, a44
	v_mov_b32_dpp v59, v116 row_shl:1 row_mask:0xf bank_mask:0xf
	v_pk_mov_b32 v[68:69], v[116:117], v[118:119] op_sel:[1,0]
	v_mov_b32_e32 v94, v57
	v_pk_fma_f32 v[62:63], v[68:69], v[58:59], v[62:63]
	s_mov_b64 s[0:1], 0x1420000
	v_pk_add_f32 v[60:61], v[60:61], v[62:63]
	v_mov_b32_dpp v94, v115 row_shr:1 row_mask:0xf bank_mask:0xf
	v_mov_b32_e32 v99, v115
	v_accvgpr_read_b32 v41, a11
	v_lshl_add_u64 v[62:63], v[54:55], 0, s[0:1]
	v_mov_b32_e32 v128, v60
	v_mov_b32_e32 v129, v61
	v_pk_mul_f32 v[60:61], v[98:99], v[94:95]
	v_accvgpr_read_b32 v40, a10
	v_mov_b32_e32 v102, v51
	v_mov_b32_dpp v57, v114 row_shl:1 row_mask:0xf bank_mask:0xf
	v_pk_fma_f32 v[60:61], v[114:115], v[40:41], v[60:61] op_sel_hi:[0,1,1]
	v_mov_b32_e32 v62, v115
	v_mov_b32_e32 v63, v101
	v_mov_b32_dpp v102, v113 row_shr:1 row_mask:0xf bank_mask:0xf
	v_mov_b32_e32 v105, v113
	v_pk_fma_f32 v[60:61], v[62:63], v[56:57], v[60:61]
	v_pk_mul_f32 v[62:63], v[104:105], v[102:103]
	v_mov_b32_dpp v51, v112 row_shl:1 row_mask:0xf bank_mask:0xf
	v_pk_fma_f32 v[62:63], v[112:113], v[4:5], v[62:63] op_sel_hi:[0,1,1]
	v_mov_b32_e32 v68, v113
	v_mov_b32_e32 v69, v123
	v_mov_b32_e32 v108, v49
	v_pk_fma_f32 v[62:63], v[68:69], v[50:51], v[62:63]
	v_pk_add_f32 v[60:61], v[60:61], 0 op_sel_hi:[1,0]
	v_mov_b32_dpp v108, v91 row_shr:1 row_mask:0xf bank_mask:0xf
	v_mov_b32_e32 v111, v91
	v_accvgpr_read_b32 v5, a3
	v_pk_add_f32 v[60:61], v[60:61], v[62:63]
	v_pk_mul_f32 v[62:63], v[110:111], v[108:109]
	v_accvgpr_read_b32 v4, a2
	v_mov_b32_dpp v49, v90 row_shl:1 row_mask:0xf bank_mask:0xf
	v_pk_fma_f32 v[62:63], v[90:91], v[4:5], v[62:63] op_sel_hi:[0,1,1]
	v_mov_b32_e32 v68, v91
	v_mov_b32_e32 v69, v119
	v_pk_fma_f32 v[62:63], v[68:69], v[48:49], v[62:63]
	s_mov_b64 s[0:1], 0x1430000
	v_pk_add_f32 v[60:61], v[60:61], v[62:63]
	v_lshl_add_u64 v[136:137], v[134:135], 0, s[0:1]
	s_nop 1
	s_mov_b64 vcc, s[28:29]
	s_nop 0
	v_cndmask_b32_dpp v130, v60, v128, vcc quad_perm:[1,0,3,2] row_mask:0xf bank_mask:0xf
	v_cndmask_b32_dpp v131, v61, v129, vcc quad_perm:[1,0,3,2] row_mask:0xf bank_mask:0xf
	s_mov_b64 vcc, s[30:31]
	s_nop 0
	v_cndmask_b32_dpp v132, v128, v60, vcc quad_perm:[1,0,3,2] row_mask:0xf bank_mask:0xf
	v_cndmask_b32_dpp v133, v129, v61, vcc quad_perm:[1,0,3,2] row_mask:0xf bank_mask:0xf
	global_store_dwordx4 v[136:137], v[130:133], off sc0 sc1 nt
	s_nop 1
	s_waitcnt vmcnt(12)
	s_waitcnt lgkmcnt(0)
	s_barrier
	v_accvgpr_read_b32 v2, a1
	v_accvgpr_read_b32 v12, a5
	ds_read_b64 v[60:61], v12
	ds_read_b64 v[62:63], v12 offset:288
	ds_read_b64 v[68:69], v12 offset:576
	ds_read_b64 v[70:71], v12 offset:1728
	ds_read_b64 v[72:73], v12 offset:2016
	ds_read_b64 v[82:83], v12 offset:2304
	ds_read_b64 v[80:81], v12 offset:3456
	ds_read_b64 v[84:85], v12 offset:3744
	ds_read_b64 v[116:117], v12 offset:4032
	ds_read_b64 v[114:115], v12 offset:5184
	ds_read_b64 v[112:113], v12 offset:5472
	ds_read_b64 v[90:91], v12 offset:5760
	ds_read_b32 v43, v2
	ds_read_b32 v19, v2 offset:288
	ds_read_b32 v39, v2 offset:576
	ds_read_b32 v25, v2 offset:1728
	ds_read_b32 v7, v2 offset:2016
	ds_read_b32 v21, v2 offset:2304
	ds_read_b32 v11, v2 offset:3456
	ds_read_b32 v35, v2 offset:3744
	ds_read_b32 v59, v2 offset:4032
	ds_read_b32 v57, v2 offset:5184
	ds_read_b32 v51, v2 offset:5472
	ds_read_b32 v49, v2 offset:5760
	s_waitcnt lgkmcnt(0)
	v_accvgpr_read_b32 v101, a23
	v_mov_b32_e32 v46, v43
	v_mov_b32_e32 v65, v61
	v_accvgpr_read_b32 v31, a25
	v_mov_b32_dpp v46, v61 row_shr:1 row_mask:0xf bank_mask:0xf
	v_pk_mul_f32 v[86:87], v[64:65], v[46:47]
	v_accvgpr_read_b32 v100, a22
	v_accvgpr_read_b32 v30, a24
	v_mov_b32_e32 v26, v19
	v_mov_b32_dpp v43, v60 row_shl:1 row_mask:0xf bank_mask:0xf
	v_pk_fma_f32 v[86:87], v[60:61], v[100:101], v[86:87] op_sel_hi:[0,1,1]
	v_pk_mov_b32 v[60:61], v[60:61], v[30:31] op_sel:[1,0]
	v_mov_b32_dpp v26, v63 row_shr:1 row_mask:0xf bank_mask:0xf
	v_mov_b32_e32 v1, v63
	v_pk_fma_f32 v[60:61], v[60:61], v[42:43], v[86:87]
	v_pk_mul_f32 v[86:87], v[0:1], v[26:27]
	v_accvgpr_read_b32 v0, a34
	v_accvgpr_mov_b32 a12, a14
	v_accvgpr_read_b32 v1, a35
	v_accvgpr_mov_b32 a13, a15
	v_mov_b32_dpp v19, v62 row_shl:1 row_mask:0xf bank_mask:0xf
	v_pk_fma_f32 v[86:87], v[62:63], v[16:17], v[86:87] op_sel_hi:[0,1,1]
	v_accvgpr_write_b32 a14, v16
	v_pk_mov_b32 v[62:63], v[62:63], v[0:1] op_sel:[1,0]
	v_mov_b32_e32 v44, v39
	v_accvgpr_write_b32 a15, v17
	v_pk_fma_f32 v[62:63], v[62:63], v[18:19], v[86:87]
	v_pk_add_f32 v[60:61], v[60:61], 0 op_sel_hi:[1,0]
	v_mov_b32_dpp v44, v69 row_shr:1 row_mask:0xf bank_mask:0xf
	v_accvgpr_read_b32 v16, a48
	v_mov_b32_e32 v17, v69
	v_accvgpr_read_b32 v67, a47
	v_pk_add_f32 v[60:61], v[60:61], v[62:63]
	v_pk_mul_f32 v[62:63], v[16:17], v[44:45]
	v_accvgpr_read_b32 v66, a46
	v_mov_b32_dpp v39, v68 row_shl:1 row_mask:0xf bank_mask:0xf
	v_pk_fma_f32 v[62:63], v[68:69], v[14:15], v[62:63] op_sel_hi:[0,1,1]
	v_pk_mov_b32 v[68:69], v[68:69], v[66:67] op_sel:[1,0]
	v_mov_b32_e32 v36, v25
	v_pk_fma_f32 v[62:63], v[68:69], v[38:39], v[62:63]
	s_mov_b64 s[0:1], 0x1800000
	v_pk_add_f32 v[60:61], v[60:61], v[62:63]
	v_mov_b32_dpp v36, v71 row_shr:1 row_mask:0xf bank_mask:0xf
	v_mov_b32_e32 v127, v71
	v_lshl_add_u64 v[62:63], v[54:55], 0, s[0:1]
	v_mov_b32_e32 v128, v60
	v_mov_b32_e32 v129, v61
	v_pk_mul_f32 v[60:61], v[126:127], v[36:37]
	v_mov_b32_e32 v12, v7
	v_mov_b32_dpp v25, v70 row_shl:1 row_mask:0xf bank_mask:0xf
	v_pk_fma_f32 v[60:61], v[70:71], v[8:9], v[60:61] op_sel_hi:[0,1,1]
	v_mov_b32_e32 v62, v71
	v_mov_b32_e32 v63, v31
	v_mov_b32_dpp v12, v73 row_shr:1 row_mask:0xf bank_mask:0xf
	v_mov_b32_e32 v75, v73
	v_pk_fma_f32 v[60:61], v[62:63], v[24:25], v[60:61]
	v_pk_mul_f32 v[62:63], v[74:75], v[12:13]
	v_mov_b32_dpp v7, v72 row_shl:1 row_mask:0xf bank_mask:0xf
	v_pk_fma_f32 v[62:63], v[72:73], v[22:23], v[62:63] op_sel_hi:[0,1,1]
	v_accvgpr_write_b32 a4, v22
	v_mov_b32_e32 v68, v73
	v_mov_b32_e32 v69, v1
	v_mov_b32_e32 v78, v21
	v_accvgpr_write_b32 a5, v23
	v_pk_fma_f32 v[62:63], v[68:69], v[6:7], v[62:63]
	v_pk_add_f32 v[60:61], v[60:61], 0 op_sel_hi:[1,0]
	v_mov_b32_dpp v78, v83 row_shr:1 row_mask:0xf bank_mask:0xf
	v_mov_b32_e32 v53, v83
	v_accvgpr_read_b32 v22, a26
	v_pk_add_f32 v[60:61], v[60:61], v[62:63]
	v_pk_mul_f32 v[62:63], v[52:53], v[78:79]
	v_accvgpr_read_b32 v23, a27
	v_mov_b32_dpp v21, v82 row_shl:1 row_mask:0xf bank_mask:0xf
	v_pk_fma_f32 v[62:63], v[82:83], v[22:23], v[62:63] op_sel_hi:[0,1,1]
	v_mov_b32_e32 v68, v83
	v_mov_b32_e32 v69, v67
	v_pk_fma_f32 v[62:63], v[68:69], v[20:21], v[62:63]
	v_mov_b32_e32 v76, v11
	v_pk_add_f32 v[60:61], v[60:61], v[62:63]
	s_mov_b64 s[0:1], 0x1810000
	v_mov_b32_dpp v76, v81 row_shr:1 row_mask:0xf bank_mask:0xf
	v_mov_b32_e32 v121, v81
	v_accvgpr_read_b32 v15, a13
	v_lshl_add_u64 v[136:137], v[134:135], 0, s[0:1]
	s_nop 1
	s_mov_b64 vcc, s[28:29]
	s_nop 0
	v_cndmask_b32_dpp v130, v60, v128, vcc quad_perm:[1,0,3,2] row_mask:0xf bank_mask:0xf
	v_cndmask_b32_dpp v131, v61, v129, vcc quad_perm:[1,0,3,2] row_mask:0xf bank_mask:0xf
	s_mov_b64 vcc, s[30:31]
	s_nop 0
	v_cndmask_b32_dpp v132, v128, v60, vcc quad_perm:[1,0,3,2] row_mask:0xf bank_mask:0xf
	v_cndmask_b32_dpp v133, v129, v61, vcc quad_perm:[1,0,3,2] row_mask:0xf bank_mask:0xf
	global_store_dwordx4 v[136:137], v[130:133], off sc0 sc1 nt
	s_nop 1
	v_pk_mul_f32 v[60:61], v[120:121], v[76:77]
	v_accvgpr_read_b32 v14, a12
	v_mov_b32_e32 v2, v35
	v_mov_b32_dpp v11, v80 row_shl:1 row_mask:0xf bank_mask:0xf
	v_pk_fma_f32 v[60:61], v[80:81], v[124:125], v[60:61] op_sel_hi:[0,1,1]
	v_pk_mov_b32 v[62:63], v[80:81], v[14:15] op_sel:[1,0]
	v_mov_b32_dpp v2, v85 row_shr:1 row_mask:0xf bank_mask:0xf
	v_mov_b32_e32 v107, v85
	v_pk_fma_f32 v[60:61], v[62:63], v[10:11], v[60:61]
	v_pk_mul_f32 v[62:63], v[106:107], v[2:3]
	v_mov_b32_dpp v35, v84 row_shl:1 row_mask:0xf bank_mask:0xf
	v_pk_fma_f32 v[62:63], v[84:85], v[28:29], v[62:63] op_sel_hi:[0,1,1]
	v_pk_mov_b32 v[68:69], v[84:85], v[122:123] op_sel:[1,0]
	v_mov_b32_e32 v92, v59
	v_pk_fma_f32 v[62:63], v[68:69], v[34:35], v[62:63]
	v_pk_add_f32 v[60:61], v[60:61], 0 op_sel_hi:[1,0]
	v_mov_b32_dpp v92, v117 row_shr:1 row_mask:0xf bank_mask:0xf
	v_mov_b32_e32 v97, v117
	v_accvgpr_read_b32 v87, a9
	v_pk_add_f32 v[60:61], v[60:61], v[62:63]
	v_pk_mul_f32 v[62:63], v[96:97], v[92:93]
	v_accvgpr_read_b32 v86, a8
	v_mov_b32_dpp v59, v116 row_shl:1 row_mask:0xf bank_mask:0xf
	v_pk_fma_f32 v[62:63], v[116:117], v[86:87], v[62:63] op_sel_hi:[0,1,1]
	v_pk_mov_b32 v[68:69], v[116:117], v[118:119] op_sel:[1,0]
	v_mov_b32_e32 v94, v57
	v_pk_fma_f32 v[62:63], v[68:69], v[58:59], v[62:63]
	s_mov_b64 s[0:1], 0x1820000
	v_pk_add_f32 v[60:61], v[60:61], v[62:63]
	v_mov_b32_dpp v94, v115 row_shr:1 row_mask:0xf bank_mask:0xf
	v_mov_b32_e32 v99, v115
	v_lshl_add_u64 v[62:63], v[54:55], 0, s[0:1]
	v_mov_b32_e32 v128, v60
	v_mov_b32_e32 v129, v61
	v_pk_mul_f32 v[60:61], v[98:99], v[94:95]
	v_mov_b32_e32 v102, v51
	v_mov_b32_dpp v57, v114 row_shl:1 row_mask:0xf bank_mask:0xf
	v_pk_fma_f32 v[60:61], v[114:115], v[40:41], v[60:61] op_sel_hi:[0,1,1]
	v_mov_b32_e32 v62, v115
	v_mov_b32_e32 v63, v15
	v_mov_b32_dpp v102, v113 row_shr:1 row_mask:0xf bank_mask:0xf
	v_mov_b32_e32 v105, v113
	v_accvgpr_read_b32 v89, a19
	v_pk_fma_f32 v[60:61], v[62:63], v[56:57], v[60:61]
	v_pk_mul_f32 v[62:63], v[104:105], v[102:103]
	v_accvgpr_read_b32 v88, a18
	v_mov_b32_dpp v51, v112 row_shl:1 row_mask:0xf bank_mask:0xf
	v_pk_fma_f32 v[62:63], v[112:113], v[88:89], v[62:63] op_sel_hi:[0,1,1]
	v_mov_b32_e32 v68, v113
	v_mov_b32_e32 v69, v123
	v_mov_b32_e32 v108, v49
	v_pk_fma_f32 v[62:63], v[68:69], v[50:51], v[62:63]
	v_pk_add_f32 v[60:61], v[60:61], 0 op_sel_hi:[1,0]
	v_mov_b32_dpp v108, v91 row_shr:1 row_mask:0xf bank_mask:0xf
	v_mov_b32_e32 v111, v91
	v_pk_add_f32 v[60:61], v[60:61], v[62:63]
	v_pk_mul_f32 v[62:63], v[110:111], v[108:109]
	v_mov_b32_dpp v49, v90 row_shl:1 row_mask:0xf bank_mask:0xf
	v_pk_fma_f32 v[62:63], v[90:91], v[4:5], v[62:63] op_sel_hi:[0,1,1]
	v_mov_b32_e32 v68, v91
	v_mov_b32_e32 v69, v119
	v_pk_fma_f32 v[62:63], v[68:69], v[48:49], v[62:63]
	s_mov_b64 s[0:1], 0x1830000
	v_pk_add_f32 v[60:61], v[60:61], v[62:63]
	v_lshl_add_u64 v[136:137], v[134:135], 0, s[0:1]
	s_nop 1
	s_mov_b64 vcc, s[28:29]
	s_nop 0
	v_cndmask_b32_dpp v130, v60, v128, vcc quad_perm:[1,0,3,2] row_mask:0xf bank_mask:0xf
	v_cndmask_b32_dpp v131, v61, v129, vcc quad_perm:[1,0,3,2] row_mask:0xf bank_mask:0xf
	s_mov_b64 vcc, s[30:31]
	s_nop 0
	v_cndmask_b32_dpp v132, v128, v60, vcc quad_perm:[1,0,3,2] row_mask:0xf bank_mask:0xf
	v_cndmask_b32_dpp v133, v129, v61, vcc quad_perm:[1,0,3,2] row_mask:0xf bank_mask:0xf
	global_store_dwordx4 v[136:137], v[130:133], off sc0 sc1 nt
	s_nop 1
	v_accvgpr_write_b32 a12, v28
	s_waitcnt vmcnt(8)
	v_accvgpr_write_b32 a13, v29
	v_mov_b64_e32 v[28:29], v[4:5]
	s_waitcnt lgkmcnt(0)
	s_barrier
	v_accvgpr_read_b32 v2, a6
	v_accvgpr_read_b32 v4, a7
	ds_read_b64 v[60:61], v2
	ds_read_b64 v[62:63], v2 offset:288
	ds_read_b64 v[68:69], v2 offset:576
	ds_read_b64 v[70:71], v2 offset:1728
	ds_read_b64 v[72:73], v2 offset:2016
	ds_read_b64 v[82:83], v2 offset:2304
	ds_read_b64 v[80:81], v2 offset:3456
	ds_read_b64 v[84:85], v2 offset:3744
	ds_read_b64 v[116:117], v2 offset:4032
	ds_read_b64 v[114:115], v2 offset:5184
	ds_read_b64 v[112:113], v2 offset:5472
	ds_read_b64 v[90:91], v2 offset:5760
	ds_read_b32 v43, v4
	ds_read_b32 v19, v4 offset:288
	ds_read_b32 v39, v4 offset:576
	ds_read_b32 v25, v4 offset:1728
	ds_read_b32 v7, v4 offset:2016
	ds_read_b32 v21, v4 offset:2304
	ds_read_b32 v11, v4 offset:3456
	ds_read_b32 v35, v4 offset:3744
	ds_read_b32 v59, v4 offset:4032
	ds_read_b32 v57, v4 offset:5184
	ds_read_b32 v51, v4 offset:5472
	ds_read_b32 v49, v4 offset:5760
	s_waitcnt lgkmcnt(0)
	v_accvgpr_read_b32 v8, a24
	v_mov_b32_e32 v46, v43
	v_mov_b32_e32 v65, v61
	v_mov_b32_e32 v26, v19
	v_mov_b32_dpp v46, v61 row_shr:1 row_mask:0xf bank_mask:0xf
	v_accvgpr_read_b32 v32, a32
	v_accvgpr_read_b32 v9, a25
	v_mov_b64_e32 v[124:125], v[40:41]
	v_pk_mul_f32 v[30:31], v[64:65], v[46:47]
	v_mov_b32_dpp v26, v63 row_shr:1 row_mask:0xf bank_mask:0xf
	v_mov_b32_e32 v33, v63
	v_accvgpr_read_b32 v4, a14
	v_accvgpr_read_b32 v41, a35
	v_mov_b32_e32 v44, v39
	v_pk_fma_f32 v[30:31], v[60:61], v[100:101], v[30:31] op_sel_hi:[0,1,1]
	v_mov_b32_dpp v43, v60 row_shl:1 row_mask:0xf bank_mask:0xf
	v_pk_mov_b32 v[46:47], v[60:61], v[8:9] op_sel:[1,0]
	v_pk_mul_f32 v[26:27], v[32:33], v[26:27]
	v_accvgpr_read_b32 v5, a15
	v_accvgpr_read_b32 v40, a34
	v_mov_b32_dpp v44, v69 row_shr:1 row_mask:0xf bank_mask:0xf
	v_mov_b32_e32 v17, v69
	v_accvgpr_read_b32 v0, a16
	v_pk_fma_f32 v[30:31], v[46:47], v[42:43], v[30:31]
	v_pk_fma_f32 v[26:27], v[62:63], v[4:5], v[26:27] op_sel_hi:[0,1,1]
	v_mov_b32_dpp v19, v62 row_shl:1 row_mask:0xf bank_mask:0xf
	v_pk_mov_b32 v[32:33], v[62:63], v[40:41] op_sel:[1,0]
	v_pk_mul_f32 v[16:17], v[16:17], v[44:45]
	v_accvgpr_read_b32 v1, a17
	v_pk_fma_f32 v[18:19], v[32:33], v[18:19], v[26:27]
	v_pk_add_f32 v[26:27], v[30:31], 0 op_sel_hi:[1,0]
	v_mov_b32_dpp v39, v68 row_shl:1 row_mask:0xf bank_mask:0xf
	v_pk_fma_f32 v[16:17], v[68:69], v[0:1], v[16:17] op_sel_hi:[0,1,1]
	v_pk_mov_b32 v[30:31], v[68:69], v[66:67] op_sel:[1,0]
	v_pk_add_f32 v[18:19], v[26:27], v[18:19]
	v_pk_fma_f32 v[16:17], v[30:31], v[38:39], v[16:17]
	v_mov_b32_e32 v36, v25
	s_mov_b64 s[0:1], 0x1c00000
	v_pk_add_f32 v[16:17], v[18:19], v[16:17]
	v_mov_b32_dpp v36, v71 row_shr:1 row_mask:0xf bank_mask:0xf
	v_mov_b32_e32 v127, v71
	v_accvgpr_read_b32 v0, a20
	v_lshl_add_u64 v[26:27], v[54:55], 0, s[0:1]
	v_mov_b32_e32 v128, v16
	v_mov_b32_e32 v129, v17
	v_mov_b32_e32 v12, v7
	v_pk_mul_f32 v[16:17], v[126:127], v[36:37]
	v_accvgpr_read_b32 v1, a21
	v_mov_b32_dpp v12, v73 row_shr:1 row_mask:0xf bank_mask:0xf
	v_pk_fma_f32 v[16:17], v[70:71], v[0:1], v[16:17] op_sel_hi:[0,1,1]
	v_mov_b32_e32 v75, v73
	v_accvgpr_read_b32 v0, a4
	v_mov_b32_e32 v78, v21
	v_pk_mul_f32 v[12:13], v[74:75], v[12:13]
	v_accvgpr_read_b32 v1, a5
	v_mov_b32_dpp v25, v70 row_shl:1 row_mask:0xf bank_mask:0xf
	v_mov_b32_dpp v7, v72 row_shl:1 row_mask:0xf bank_mask:0xf
	v_mov_b32_dpp v78, v83 row_shr:1 row_mask:0xf bank_mask:0xf
	v_mov_b32_e32 v8, v71
	v_pk_fma_f32 v[12:13], v[72:73], v[0:1], v[12:13] op_sel_hi:[0,1,1]
	v_mov_b32_e32 v5, v41
	v_mov_b32_e32 v4, v73
	v_mov_b32_e32 v53, v83
	v_pk_fma_f32 v[16:17], v[8:9], v[24:25], v[16:17]
	v_pk_fma_f32 v[6:7], v[4:5], v[6:7], v[12:13]
	v_pk_mul_f32 v[12:13], v[52:53], v[78:79]
	v_mov_b32_dpp v21, v82 row_shl:1 row_mask:0xf bank_mask:0xf
	v_pk_add_f32 v[16:17], v[16:17], 0 op_sel_hi:[1,0]
	v_pk_fma_f32 v[12:13], v[82:83], v[22:23], v[12:13] op_sel_hi:[0,1,1]
	v_mov_b32_e32 v66, v83
	v_pk_add_f32 v[6:7], v[16:17], v[6:7]
	v_pk_fma_f32 v[12:13], v[66:67], v[20:21], v[12:13]
	v_mov_b32_e32 v76, v11
	v_pk_add_f32 v[6:7], v[6:7], v[12:13]
	s_mov_b64 s[0:1], 0x1c10000
	v_mov_b32_dpp v76, v81 row_shr:1 row_mask:0xf bank_mask:0xf
	v_mov_b32_e32 v121, v81
	v_accvgpr_read_b32 v0, a36
	v_lshl_add_u64 v[136:137], v[134:135], 0, s[0:1]
	s_nop 1
	s_mov_b64 vcc, s[28:29]
	s_nop 0
	v_cndmask_b32_dpp v130, v6, v128, vcc quad_perm:[1,0,3,2] row_mask:0xf bank_mask:0xf
	v_cndmask_b32_dpp v131, v7, v129, vcc quad_perm:[1,0,3,2] row_mask:0xf bank_mask:0xf
	s_mov_b64 vcc, s[30:31]
	s_nop 0
	v_cndmask_b32_dpp v132, v128, v6, vcc quad_perm:[1,0,3,2] row_mask:0xf bank_mask:0xf
	v_cndmask_b32_dpp v133, v129, v7, vcc quad_perm:[1,0,3,2] row_mask:0xf bank_mask:0xf
	global_store_dwordx4 v[136:137], v[130:133], off sc0 sc1 nt
	s_nop 1
	v_mov_b32_e32 v2, v35
	v_pk_mul_f32 v[6:7], v[120:121], v[76:77]
	v_accvgpr_read_b32 v1, a37
	v_mov_b32_dpp v2, v85 row_shr:1 row_mask:0xf bank_mask:0xf
	v_pk_fma_f32 v[6:7], v[80:81], v[0:1], v[6:7] op_sel_hi:[0,1,1]
	v_mov_b32_e32 v107, v85
	v_accvgpr_read_b32 v0, a12
	v_mov_b32_e32 v92, v59
	v_pk_mul_f32 v[2:3], v[106:107], v[2:3]
	v_accvgpr_read_b32 v1, a13
	v_mov_b32_dpp v11, v80 row_shl:1 row_mask:0xf bank_mask:0xf
	v_mov_b32_dpp v35, v84 row_shl:1 row_mask:0xf bank_mask:0xf
	v_mov_b32_dpp v92, v117 row_shr:1 row_mask:0xf bank_mask:0xf
	v_pk_mov_b32 v[8:9], v[80:81], v[14:15] op_sel:[1,0]
	v_pk_fma_f32 v[2:3], v[84:85], v[0:1], v[2:3] op_sel_hi:[0,1,1]
	v_pk_mov_b32 v[4:5], v[84:85], v[122:123] op_sel:[1,0]
	v_mov_b32_e32 v97, v117
	v_pk_fma_f32 v[6:7], v[8:9], v[10:11], v[6:7]
	v_pk_fma_f32 v[0:1], v[4:5], v[34:35], v[2:3]
	v_pk_mul_f32 v[2:3], v[96:97], v[92:93]
	v_mov_b32_dpp v59, v116 row_shl:1 row_mask:0xf bank_mask:0xf
	v_pk_add_f32 v[6:7], v[6:7], 0 op_sel_hi:[1,0]
	v_pk_fma_f32 v[2:3], v[116:117], v[86:87], v[2:3] op_sel_hi:[0,1,1]
	v_pk_mov_b32 v[4:5], v[116:117], v[118:119] op_sel:[1,0]
	v_pk_add_f32 v[0:1], v[6:7], v[0:1]
	v_pk_fma_f32 v[2:3], v[4:5], v[58:59], v[2:3]
	v_mov_b32_e32 v94, v57
	v_pk_add_f32 v[0:1], v[0:1], v[2:3]
	s_mov_b64 s[0:1], 0x1c20000
	v_mov_b32_dpp v94, v115 row_shr:1 row_mask:0xf bank_mask:0xf
	v_mov_b32_e32 v102, v51
	v_mov_b32_e32 v99, v115
	v_lshl_add_u64 v[2:3], v[54:55], 0, s[0:1]
	v_mov_b32_e32 v128, v0
	v_mov_b32_e32 v129, v1
	v_mov_b32_dpp v102, v113 row_shr:1 row_mask:0xf bank_mask:0xf
	v_pk_mul_f32 v[0:1], v[98:99], v[94:95]
	v_mov_b32_e32 v105, v113
	v_mov_b32_dpp v57, v114 row_shl:1 row_mask:0xf bank_mask:0xf
	v_pk_fma_f32 v[0:1], v[114:115], v[124:125], v[0:1] op_sel_hi:[0,1,1]
	v_mov_b32_e32 v14, v115
	v_pk_mul_f32 v[2:3], v[104:105], v[102:103]
	v_mov_b32_dpp v51, v112 row_shl:1 row_mask:0xf bank_mask:0xf
	v_mov_b32_e32 v108, v49
	v_pk_fma_f32 v[0:1], v[14:15], v[56:57], v[0:1]
	v_pk_fma_f32 v[2:3], v[112:113], v[88:89], v[2:3] op_sel_hi:[0,1,1]
	v_mov_b32_e32 v122, v113
	v_mov_b32_dpp v108, v91 row_shr:1 row_mask:0xf bank_mask:0xf
	v_pk_add_f32 v[0:1], v[0:1], 0 op_sel_hi:[1,0]
	v_pk_fma_f32 v[2:3], v[122:123], v[50:51], v[2:3]
	v_mov_b32_e32 v111, v91
	v_pk_add_f32 v[0:1], v[0:1], v[2:3]
	v_pk_mul_f32 v[2:3], v[110:111], v[108:109]
	v_mov_b32_dpp v49, v90 row_shl:1 row_mask:0xf bank_mask:0xf
	v_pk_fma_f32 v[2:3], v[90:91], v[28:29], v[2:3] op_sel_hi:[0,1,1]
	v_mov_b32_e32 v118, v91
	v_pk_fma_f32 v[2:3], v[118:119], v[48:49], v[2:3]
	s_mov_b64 s[0:1], 0x1c30000
	v_pk_add_f32 v[0:1], v[0:1], v[2:3]
	v_lshl_add_u64 v[136:137], v[134:135], 0, s[0:1]
	s_nop 1
	s_mov_b64 vcc, s[28:29]
	s_nop 0
	v_cndmask_b32_dpp v130, v0, v128, vcc quad_perm:[1,0,3,2] row_mask:0xf bank_mask:0xf
	v_cndmask_b32_dpp v131, v1, v129, vcc quad_perm:[1,0,3,2] row_mask:0xf bank_mask:0xf
	s_mov_b64 vcc, s[30:31]
	s_nop 0
	v_cndmask_b32_dpp v132, v128, v0, vcc quad_perm:[1,0,3,2] row_mask:0xf bank_mask:0xf
	v_cndmask_b32_dpp v133, v129, v1, vcc quad_perm:[1,0,3,2] row_mask:0xf bank_mask:0xf
	global_store_dwordx4 v[136:137], v[130:133], off sc0 sc1 nt
	s_nop 1
	s_endpgm
